# GEMM K-loops: per-unit accumulator zeroing (128 v_mov) removed by peeling the first K-loop iteration with srcC=0 on each accumulator's first MFMA (bitwise identical)
# speedup vs baseline: 1.0078x; 1.0078x over previous
.LBB0_296:
	s_ashr_i32 s15, s14, 31
	s_lshl_b64 s[16:17], s[14:15], 19
	s_add_u32 s16, s31, s16
	s_addc_u32 s17, s35, s17
	s_and_b64 s[18:19], s[38:39], exec
	s_cselect_b32 s15, s17, s21
	s_cselect_b32 s51, s16, s20
	s_ashr_i32 s13, s12, 31
	s_lshl_b64 s[18:19], s[12:13], 19
	s_add_u32 s18, s36, s18
	s_addc_u32 s19, s37, s19
	s_and_b64 s[26:27], s[38:39], exec
	s_cselect_b32 s13, s19, s23
	s_cselect_b32 s52, s18, s22
	s_add_u32 s53, s22, 0x100
	s_addc_u32 s54, s23, 0
	s_mov_b32 s55, -2
	s_add_u32 s22, s20, 0x100
	s_addc_u32 s23, s21, 0
	s_add_i32 s56, 0, 0x10000
	s_cmp_eq_u32 s55, 12
	s_cselect_b32 s41, s15, s23
	s_cselect_b32 s40, s51, s22
	v_add_u32_e32 v2, s56, v205
	s_cselect_b32 s27, s13, s54
	s_cselect_b32 s26, s52, s53
	s_add_i32 s57, 0, 0x14000
	ds_read_b128 v[132:135], v2
	ds_read_b128 v[136:139], v2 offset:1024
	ds_read_b128 v[140:143], v2 offset:2048
	ds_read_b128 v[144:147], v2 offset:3072
	v_add_u32_e32 v2, s57, v205
	ds_read_b128 v[148:151], v2
	ds_read_b128 v[152:155], v2 offset:1024
	ds_read_b128 v[156:159], v2 offset:2048
	ds_read_b128 v[160:163], v2 offset:3072
	v_lshl_add_u64 v[214:215], s[20:21], 0, v[212:213]
	s_add_i32 m0, s44, 0xc000
	ds_read_b128 v[164:167], v207
	ds_read_b128 v[168:171], v207 offset:1024
	ds_read_b128 v[172:175], v207 offset:2048
	ds_read_b128 v[176:179], v207 offset:3072
	ds_read_b128 v[180:183], v207 offset:4096
	ds_read_b128 v[184:187], v207 offset:5120
	ds_read_b128 v[188:191], v207 offset:6144
	ds_read_b128 v[192:195], v207 offset:7168
	global_load_lds_dwordx4 v[214:215], off
	v_lshl_add_u64 v[214:215], s[20:21], 0, v[210:211]
	s_add_i32 m0, s44, 0xe000
	s_nop 0
	global_load_lds_dwordx4 v[214:215], off
	s_waitcnt vmcnt(8)
	s_waitcnt lgkmcnt(0)
	s_barrier
	s_setprio 1
	s_waitcnt lgkmcnt(0)
	v_mfma_f32_16x16x32_bf16 v[128:131], v[132:135], v[164:167], 0
	v_mfma_f32_16x16x32_bf16 v[124:127], v[140:143], v[164:167], 0
	v_mfma_f32_16x16x32_bf16 v[112:115], v[132:135], v[172:175], 0
	v_mfma_f32_16x16x32_bf16 v[108:111], v[140:143], v[172:175], 0
	v_mfma_f32_16x16x32_bf16 v[96:99], v[132:135], v[180:183], 0
	v_mfma_f32_16x16x32_bf16 v[92:95], v[140:143], v[180:183], 0
	v_mfma_f32_16x16x32_bf16 v[80:83], v[132:135], v[188:191], 0
	v_mfma_f32_16x16x32_bf16 v[76:79], v[140:143], v[188:191], 0
	v_mfma_f32_16x16x32_bf16 v[128:131], v[136:139], v[168:171], v[128:131]
	v_mfma_f32_16x16x32_bf16 v[124:127], v[144:147], v[168:171], v[124:127]
	v_mfma_f32_16x16x32_bf16 v[112:115], v[136:139], v[176:179], v[112:115]
	v_mfma_f32_16x16x32_bf16 v[108:111], v[144:147], v[176:179], v[108:111]
	v_mfma_f32_16x16x32_bf16 v[96:99], v[136:139], v[184:187], v[96:99]
	v_mfma_f32_16x16x32_bf16 v[92:95], v[144:147], v[184:187], v[92:95]
	v_mfma_f32_16x16x32_bf16 v[80:83], v[136:139], v[192:195], v[80:83]
	v_mfma_f32_16x16x32_bf16 v[76:79], v[144:147], v[192:195], v[76:79]
	s_setprio 0
	s_setprio 1
	v_mfma_f32_16x16x32_bf16 v[120:123], v[148:151], v[164:167], 0
	v_mfma_f32_16x16x32_bf16 v[116:119], v[156:159], v[164:167], 0
	v_mfma_f32_16x16x32_bf16 v[104:107], v[148:151], v[172:175], 0
	v_mfma_f32_16x16x32_bf16 v[100:103], v[156:159], v[172:175], 0
	v_mfma_f32_16x16x32_bf16 v[88:91], v[148:151], v[180:183], 0
	v_mfma_f32_16x16x32_bf16 v[84:87], v[156:159], v[180:183], 0
	v_mfma_f32_16x16x32_bf16 v[72:75], v[148:151], v[188:191], 0
	v_mfma_f32_16x16x32_bf16 v[68:71], v[156:159], v[188:191], 0
	v_mfma_f32_16x16x32_bf16 v[120:123], v[152:155], v[168:171], v[120:123]
	v_mfma_f32_16x16x32_bf16 v[116:119], v[160:163], v[168:171], v[116:119]
	v_mfma_f32_16x16x32_bf16 v[104:107], v[152:155], v[176:179], v[104:107]
	v_mfma_f32_16x16x32_bf16 v[100:103], v[160:163], v[176:179], v[100:103]
	v_mfma_f32_16x16x32_bf16 v[88:91], v[152:155], v[184:187], v[88:91]
	v_mfma_f32_16x16x32_bf16 v[84:87], v[160:163], v[184:187], v[84:87]
	v_mfma_f32_16x16x32_bf16 v[72:75], v[152:155], v[192:195], v[72:75]
	v_mfma_f32_16x16x32_bf16 v[68:71], v[160:163], v[192:195], v[68:71]
	s_setprio 0
	s_barrier
	s_add_i32 s20, s56, s42
	v_lshl_add_u64 v[214:215], s[26:27], 0, v[198:199]
	s_mov_b32 m0, s20
	ds_read_b128 v[164:167], v207 offset:16384
	ds_read_b128 v[168:171], v207 offset:17408
	ds_read_b128 v[172:175], v207 offset:18432
	ds_read_b128 v[176:179], v207 offset:19456
	ds_read_b128 v[180:183], v207 offset:20480
	ds_read_b128 v[184:187], v207 offset:21504
	ds_read_b128 v[188:191], v207 offset:22528
	ds_read_b128 v[192:195], v207 offset:23552
	global_load_lds_dwordx4 v[214:215], off
	s_add_i32 m0, s20, 0x2000
	s_add_u32 s20, s26, 0x40000
	v_lshl_add_u64 v[216:217], s[26:27], 0, v[0:1]
	s_addc_u32 s21, s27, 0
	s_add_i32 s56, s57, s42
	global_load_lds_dwordx4 v[216:217], off
	v_lshl_add_u64 v[218:219], s[20:21], 0, v[198:199]
	s_mov_b32 m0, s56
	v_lshl_add_u64 v[220:221], s[40:41], 0, v[196:197]
	global_load_lds_dwordx4 v[218:219], off
	v_lshl_add_u64 v[218:219], s[20:21], 0, v[0:1]
	s_add_i32 m0, s56, 0x2000
	s_nop 0
	global_load_lds_dwordx4 v[218:219], off
	v_lshl_add_u64 v[218:219], s[40:41], 0, v[200:201]
	s_mov_b32 m0, s44
	s_nop 0
	global_load_lds_dwordx4 v[218:219], off
	s_mov_b32 m0, s45
	s_nop 0
	global_load_lds_dwordx4 v[220:221], off
	s_waitcnt vmcnt(8)
	s_waitcnt lgkmcnt(0)
	s_barrier
	s_setprio 1
	s_waitcnt lgkmcnt(0)
	v_mfma_f32_16x16x32_bf16 v[64:67], v[132:135], v[164:167], 0
	v_mfma_f32_16x16x32_bf16 v[60:63], v[140:143], v[164:167], 0
	v_mfma_f32_16x16x32_bf16 v[48:51], v[132:135], v[172:175], 0
	v_mfma_f32_16x16x32_bf16 v[44:47], v[140:143], v[172:175], 0
	v_mfma_f32_16x16x32_bf16 v[32:35], v[132:135], v[180:183], 0
	v_mfma_f32_16x16x32_bf16 v[28:31], v[140:143], v[180:183], 0
	v_mfma_f32_16x16x32_bf16 v[16:19], v[132:135], v[188:191], 0
	v_mfma_f32_16x16x32_bf16 v[12:15], v[140:143], v[188:191], 0
	v_mfma_f32_16x16x32_bf16 v[64:67], v[136:139], v[168:171], v[64:67]
	v_mfma_f32_16x16x32_bf16 v[60:63], v[144:147], v[168:171], v[60:63]
	v_mfma_f32_16x16x32_bf16 v[48:51], v[136:139], v[176:179], v[48:51]
	v_mfma_f32_16x16x32_bf16 v[44:47], v[144:147], v[176:179], v[44:47]
	v_mfma_f32_16x16x32_bf16 v[32:35], v[136:139], v[184:187], v[32:35]
	v_mfma_f32_16x16x32_bf16 v[28:31], v[144:147], v[184:187], v[28:31]
	v_mfma_f32_16x16x32_bf16 v[16:19], v[136:139], v[192:195], v[16:19]
	v_mfma_f32_16x16x32_bf16 v[12:15], v[144:147], v[192:195], v[12:15]
	s_setprio 0
	s_setprio 1
	v_mfma_f32_16x16x32_bf16 v[56:59], v[148:151], v[164:167], 0
	v_mfma_f32_16x16x32_bf16 v[52:55], v[156:159], v[164:167], 0
	v_mfma_f32_16x16x32_bf16 v[40:43], v[148:151], v[172:175], 0
	v_mfma_f32_16x16x32_bf16 v[36:39], v[156:159], v[172:175], 0
	v_mfma_f32_16x16x32_bf16 v[24:27], v[148:151], v[180:183], 0
	v_mfma_f32_16x16x32_bf16 v[20:23], v[156:159], v[180:183], 0
	v_mfma_f32_16x16x32_bf16 v[8:11], v[148:151], v[188:191], 0
	v_mfma_f32_16x16x32_bf16 v[4:7], v[156:159], v[188:191], 0
	v_mfma_f32_16x16x32_bf16 v[56:59], v[152:155], v[168:171], v[56:59]
	v_mfma_f32_16x16x32_bf16 v[52:55], v[160:163], v[168:171], v[52:55]
	v_mfma_f32_16x16x32_bf16 v[40:43], v[152:155], v[176:179], v[40:43]
	v_mfma_f32_16x16x32_bf16 v[36:39], v[160:163], v[176:179], v[36:39]
	v_mfma_f32_16x16x32_bf16 v[24:27], v[152:155], v[184:187], v[24:27]
	v_mfma_f32_16x16x32_bf16 v[20:23], v[160:163], v[184:187], v[20:23]
	v_mfma_f32_16x16x32_bf16 v[8:11], v[152:155], v[192:195], v[8:11]
	v_mfma_f32_16x16x32_bf16 v[4:7], v[160:163], v[192:195], v[4:7]
	s_setprio 0
	s_barrier
	s_add_i32 s56, 0, 0x18000
	v_add_u32_e32 v2, s56, v205
	s_add_i32 s57, 0, 0x1c000
	ds_read_b128 v[132:135], v2
	ds_read_b128 v[136:139], v2 offset:1024
	ds_read_b128 v[140:143], v2 offset:2048
	ds_read_b128 v[144:147], v2 offset:3072
	v_add_u32_e32 v2, s57, v205
	ds_read_b128 v[148:151], v2
	ds_read_b128 v[152:155], v2 offset:1024
	ds_read_b128 v[156:159], v2 offset:2048
	ds_read_b128 v[160:163], v2 offset:3072
	s_add_u32 s20, s40, 0x40000
	s_addc_u32 s21, s41, 0
	s_mov_b32 m0, s46
	v_lshl_add_u64 v[222:223], s[20:21], 0, v[200:201]
	ds_read_b128 v[164:167], v207 offset:32768
	ds_read_b128 v[168:171], v207 offset:33792
	ds_read_b128 v[172:175], v207 offset:34816
	ds_read_b128 v[176:179], v207 offset:35840
	ds_read_b128 v[180:183], v207 offset:36864
	ds_read_b128 v[184:187], v207 offset:37888
	ds_read_b128 v[188:191], v207 offset:38912
	ds_read_b128 v[192:195], v207 offset:39936
	global_load_lds_dwordx4 v[222:223], off
	v_lshl_add_u64 v[222:223], s[20:21], 0, v[196:197]
	s_mov_b32 m0, s47
	s_nop 0
	global_load_lds_dwordx4 v[222:223], off
	s_waitcnt vmcnt(8)
	s_waitcnt lgkmcnt(0)
	s_barrier
	s_setprio 1
	s_waitcnt lgkmcnt(0)
	v_mfma_f32_16x16x32_bf16 v[128:131], v[132:135], v[164:167], v[128:131]
	v_mfma_f32_16x16x32_bf16 v[124:127], v[140:143], v[164:167], v[124:127]
	v_mfma_f32_16x16x32_bf16 v[112:115], v[132:135], v[172:175], v[112:115]
	v_mfma_f32_16x16x32_bf16 v[108:111], v[140:143], v[172:175], v[108:111]
	v_mfma_f32_16x16x32_bf16 v[96:99], v[132:135], v[180:183], v[96:99]
	v_mfma_f32_16x16x32_bf16 v[92:95], v[140:143], v[180:183], v[92:95]
	v_mfma_f32_16x16x32_bf16 v[80:83], v[132:135], v[188:191], v[80:83]
	v_mfma_f32_16x16x32_bf16 v[76:79], v[140:143], v[188:191], v[76:79]
	v_mfma_f32_16x16x32_bf16 v[128:131], v[136:139], v[168:171], v[128:131]
	v_mfma_f32_16x16x32_bf16 v[124:127], v[144:147], v[168:171], v[124:127]
	v_mfma_f32_16x16x32_bf16 v[112:115], v[136:139], v[176:179], v[112:115]
	v_mfma_f32_16x16x32_bf16 v[108:111], v[144:147], v[176:179], v[108:111]
	v_mfma_f32_16x16x32_bf16 v[96:99], v[136:139], v[184:187], v[96:99]
	v_mfma_f32_16x16x32_bf16 v[92:95], v[144:147], v[184:187], v[92:95]
	v_mfma_f32_16x16x32_bf16 v[80:83], v[136:139], v[192:195], v[80:83]
	v_mfma_f32_16x16x32_bf16 v[76:79], v[144:147], v[192:195], v[76:79]
	s_setprio 0
	s_setprio 1
	v_mfma_f32_16x16x32_bf16 v[120:123], v[148:151], v[164:167], v[120:123]
	v_mfma_f32_16x16x32_bf16 v[116:119], v[156:159], v[164:167], v[116:119]
	v_mfma_f32_16x16x32_bf16 v[104:107], v[148:151], v[172:175], v[104:107]
	v_mfma_f32_16x16x32_bf16 v[100:103], v[156:159], v[172:175], v[100:103]
	v_mfma_f32_16x16x32_bf16 v[88:91], v[148:151], v[180:183], v[88:91]
	v_mfma_f32_16x16x32_bf16 v[84:87], v[156:159], v[180:183], v[84:87]
	v_mfma_f32_16x16x32_bf16 v[72:75], v[148:151], v[188:191], v[72:75]
	v_mfma_f32_16x16x32_bf16 v[68:71], v[156:159], v[188:191], v[68:71]
	v_mfma_f32_16x16x32_bf16 v[120:123], v[152:155], v[168:171], v[120:123]
	v_mfma_f32_16x16x32_bf16 v[116:119], v[160:163], v[168:171], v[116:119]
	v_mfma_f32_16x16x32_bf16 v[104:107], v[152:155], v[176:179], v[104:107]
	v_mfma_f32_16x16x32_bf16 v[100:103], v[160:163], v[176:179], v[100:103]
	v_mfma_f32_16x16x32_bf16 v[88:91], v[152:155], v[184:187], v[88:91]
	v_mfma_f32_16x16x32_bf16 v[84:87], v[160:163], v[184:187], v[84:87]
	v_mfma_f32_16x16x32_bf16 v[72:75], v[152:155], v[192:195], v[72:75]
	v_mfma_f32_16x16x32_bf16 v[68:71], v[160:163], v[192:195], v[68:71]
	s_setprio 0
	s_barrier
	s_add_i32 s20, s56, s42
	v_lshl_add_u64 v[214:215], v[214:215], 0, s[28:29]
	s_mov_b32 m0, s20
	ds_read_b128 v[164:167], v207 offset:49152
	ds_read_b128 v[168:171], v207 offset:50176
	ds_read_b128 v[172:175], v207 offset:51200
	ds_read_b128 v[176:179], v207 offset:52224
	ds_read_b128 v[180:183], v207 offset:53248
	ds_read_b128 v[184:187], v207 offset:54272
	ds_read_b128 v[188:191], v207 offset:55296
	ds_read_b128 v[192:195], v207 offset:56320
	global_load_lds_dwordx4 v[214:215], off
	s_add_i32 m0, s20, 0x2000
	s_add_u32 s20, s26, 0x40080
	v_lshl_add_u64 v[214:215], v[216:217], 0, s[28:29]
	s_addc_u32 s21, s27, 0
	s_add_i32 s26, s57, s42
	global_load_lds_dwordx4 v[214:215], off
	v_lshl_add_u64 v[214:215], s[20:21], 0, v[198:199]
	s_mov_b32 m0, s26
	s_nop 0
	global_load_lds_dwordx4 v[214:215], off
	v_lshl_add_u64 v[214:215], s[20:21], 0, v[0:1]
	s_add_i32 m0, s26, 0x2000
	s_nop 0
	global_load_lds_dwordx4 v[214:215], off
	v_lshl_add_u64 v[214:215], v[218:219], 0, s[28:29]
	s_mov_b32 m0, s48
	s_nop 0
	global_load_lds_dwordx4 v[214:215], off
	v_lshl_add_u64 v[214:215], v[220:221], 0, s[28:29]
	s_mov_b32 m0, s49
	s_nop 0
	global_load_lds_dwordx4 v[214:215], off
	s_waitcnt vmcnt(8)
	s_waitcnt lgkmcnt(0)
	s_barrier
	s_setprio 1
	s_waitcnt lgkmcnt(0)
	v_mfma_f32_16x16x32_bf16 v[64:67], v[132:135], v[164:167], v[64:67]
	v_mfma_f32_16x16x32_bf16 v[60:63], v[140:143], v[164:167], v[60:63]
	v_mfma_f32_16x16x32_bf16 v[48:51], v[132:135], v[172:175], v[48:51]
	v_mfma_f32_16x16x32_bf16 v[44:47], v[140:143], v[172:175], v[44:47]
	v_mfma_f32_16x16x32_bf16 v[32:35], v[132:135], v[180:183], v[32:35]
	v_mfma_f32_16x16x32_bf16 v[28:31], v[140:143], v[180:183], v[28:31]
	v_mfma_f32_16x16x32_bf16 v[16:19], v[132:135], v[188:191], v[16:19]
	v_mfma_f32_16x16x32_bf16 v[12:15], v[140:143], v[188:191], v[12:15]
	v_mfma_f32_16x16x32_bf16 v[64:67], v[136:139], v[168:171], v[64:67]
	v_mfma_f32_16x16x32_bf16 v[60:63], v[144:147], v[168:171], v[60:63]
	v_mfma_f32_16x16x32_bf16 v[48:51], v[136:139], v[176:179], v[48:51]
	v_mfma_f32_16x16x32_bf16 v[44:47], v[144:147], v[176:179], v[44:47]
	v_mfma_f32_16x16x32_bf16 v[32:35], v[136:139], v[184:187], v[32:35]
	v_mfma_f32_16x16x32_bf16 v[28:31], v[144:147], v[184:187], v[28:31]
	v_mfma_f32_16x16x32_bf16 v[16:19], v[136:139], v[192:195], v[16:19]
	v_mfma_f32_16x16x32_bf16 v[12:15], v[144:147], v[192:195], v[12:15]
	s_setprio 0
	s_setprio 1
	v_mfma_f32_16x16x32_bf16 v[56:59], v[148:151], v[164:167], v[56:59]
	v_mfma_f32_16x16x32_bf16 v[52:55], v[156:159], v[164:167], v[52:55]
	v_mfma_f32_16x16x32_bf16 v[40:43], v[148:151], v[172:175], v[40:43]
	v_mfma_f32_16x16x32_bf16 v[36:39], v[156:159], v[172:175], v[36:39]
	v_mfma_f32_16x16x32_bf16 v[24:27], v[148:151], v[180:183], v[24:27]
	v_mfma_f32_16x16x32_bf16 v[20:23], v[156:159], v[180:183], v[20:23]
	v_mfma_f32_16x16x32_bf16 v[8:11], v[148:151], v[188:191], v[8:11]
	v_mfma_f32_16x16x32_bf16 v[4:7], v[156:159], v[188:191], v[4:7]
	v_mfma_f32_16x16x32_bf16 v[56:59], v[152:155], v[168:171], v[56:59]
	v_mfma_f32_16x16x32_bf16 v[52:55], v[160:163], v[168:171], v[52:55]
	v_mfma_f32_16x16x32_bf16 v[40:43], v[152:155], v[176:179], v[40:43]
	v_mfma_f32_16x16x32_bf16 v[36:39], v[160:163], v[176:179], v[36:39]
	v_mfma_f32_16x16x32_bf16 v[24:27], v[152:155], v[184:187], v[24:27]
	v_mfma_f32_16x16x32_bf16 v[20:23], v[160:163], v[184:187], v[20:23]
	v_mfma_f32_16x16x32_bf16 v[8:11], v[152:155], v[192:195], v[8:11]
	v_mfma_f32_16x16x32_bf16 v[4:7], v[160:163], v[192:195], v[4:7]
	s_setprio 0
	s_barrier
	s_add_i32 s55, s55, 2
	s_add_u32 s53, s53, 0x100
	s_addc_u32 s54, s54, 0
	s_cmp_gt_u32 s55, 13
	s_mov_b64 s[20:21], s[22:23]
	s_cbranch_scc1 .Lmy_gx0

.Lmy_gx0:
	s_and_b64 vcc, exec, s[8:9]
	s_cbranch_vccz .LBB0_300
	s_barrier

.LBB0_825:
	s_ashr_i32 s15, s14, 31
	s_lshl_b64 s[18:19], s[14:15], 19
	s_add_u32 s13, s35, s18
	s_addc_u32 s15, s36, s19
	s_and_b64 s[18:19], s[38:39], exec
	s_cselect_b32 s19, s15, s23
	s_cselect_b32 s18, s13, s22
	s_ashr_i32 s13, s12, 31
	s_lshl_b64 s[20:21], s[12:13], 19
	s_add_u32 s13, s37, s20
	s_addc_u32 s15, s44, s21
	s_and_b64 s[20:21], s[38:39], exec
	s_cselect_b32 s21, s15, s27
	s_cselect_b32 s20, s13, s26
	s_add_u32 s13, s26, 0x100
	v_mov_b32_e32 v218, 0x3ecc95a3
	s_addc_u32 s15, s27, 0
	s_mov_b32 s58, -2
	s_add_u32 s26, s22, 0x100
	s_addc_u32 s27, s23, 0
	s_add_i32 s59, 0, 0x10000
	s_cmp_eq_u32 s58, 12
	s_cselect_b32 s43, s19, s27
	s_cselect_b32 s42, s18, s26
	s_cselect_b32 s41, s21, s15
	s_cselect_b32 s40, s20, s13
	s_add_i32 s60, 0, 0x14000
	v_add_u32_e32 v128, s59, v179
	v_add_u32_e32 v160, s60, v179
	ds_read_b128 v[116:119], v128
	ds_read_b128 v[120:123], v128 offset:1024
	ds_read_b128 v[124:127], v128 offset:2048
	ds_read_b128 v[128:131], v128 offset:3072
	ds_read_b128 v[148:151], v160
	ds_read_b128 v[152:155], v160 offset:1024
	ds_read_b128 v[156:159], v160 offset:2048
	ds_read_b128 v[160:163], v160 offset:3072
	v_lshl_add_u64 v[176:177], s[22:23], 0, v[170:171]
	s_add_i32 m0, s46, 0xc000
	ds_read_b128 v[172:175], v181
	ds_read_b128 v[182:185], v181 offset:1024
	ds_read_b128 v[186:189], v181 offset:2048
	ds_read_b128 v[190:193], v181 offset:3072
	ds_read_b128 v[194:197], v181 offset:4096
	ds_read_b128 v[198:201], v181 offset:5120
	ds_read_b128 v[202:205], v181 offset:6144
	ds_read_b128 v[206:209], v181 offset:7168
	global_load_lds_dwordx4 v[176:177], off
	v_lshl_add_u64 v[176:177], s[22:23], 0, v[168:169]
	s_add_i32 m0, s46, 0xe000
	s_nop 0
	global_load_lds_dwordx4 v[176:177], off
	s_waitcnt vmcnt(8)
	s_waitcnt lgkmcnt(0)
	s_barrier
	s_setprio 1
	s_waitcnt lgkmcnt(0)
	v_mfma_f32_16x16x32_bf16 v[144:147], v[116:119], v[172:175], 0
	v_mfma_f32_16x16x32_bf16 v[140:143], v[124:127], v[172:175], 0
	v_mfma_f32_16x16x32_bf16 v[112:115], v[116:119], v[186:189], 0
	v_mfma_f32_16x16x32_bf16 v[108:111], v[124:127], v[186:189], 0
	v_mfma_f32_16x16x32_bf16 v[100:103], v[116:119], v[194:197], 0
	v_mfma_f32_16x16x32_bf16 v[92:95], v[124:127], v[194:197], 0
	v_mfma_f32_16x16x32_bf16 v[84:87], v[116:119], v[202:205], 0
	v_mfma_f32_16x16x32_bf16 v[76:79], v[124:127], v[202:205], 0
	v_mfma_f32_16x16x32_bf16 v[144:147], v[120:123], v[182:185], v[144:147]
	v_mfma_f32_16x16x32_bf16 v[140:143], v[128:131], v[182:185], v[140:143]
	v_mfma_f32_16x16x32_bf16 v[112:115], v[120:123], v[190:193], v[112:115]
	v_mfma_f32_16x16x32_bf16 v[108:111], v[128:131], v[190:193], v[108:111]
	v_mfma_f32_16x16x32_bf16 v[100:103], v[120:123], v[198:201], v[100:103]
	v_mfma_f32_16x16x32_bf16 v[92:95], v[128:131], v[198:201], v[92:95]
	v_mfma_f32_16x16x32_bf16 v[84:87], v[120:123], v[206:209], v[84:87]
	v_mfma_f32_16x16x32_bf16 v[76:79], v[128:131], v[206:209], v[76:79]
	s_setprio 0
	s_setprio 1
	v_mfma_f32_16x16x32_bf16 v[136:139], v[148:151], v[172:175], 0
	v_mfma_f32_16x16x32_bf16 v[132:135], v[156:159], v[172:175], 0
	v_mfma_f32_16x16x32_bf16 v[104:107], v[148:151], v[186:189], 0
	v_mfma_f32_16x16x32_bf16 v[96:99], v[156:159], v[186:189], 0
	v_mfma_f32_16x16x32_bf16 v[88:91], v[148:151], v[194:197], 0
	v_mfma_f32_16x16x32_bf16 v[80:83], v[156:159], v[194:197], 0
	v_mfma_f32_16x16x32_bf16 v[72:75], v[148:151], v[202:205], 0
	v_mfma_f32_16x16x32_bf16 v[68:71], v[156:159], v[202:205], 0
	v_mfma_f32_16x16x32_bf16 v[136:139], v[152:155], v[182:185], v[136:139]
	v_mfma_f32_16x16x32_bf16 v[132:135], v[160:163], v[182:185], v[132:135]
	v_mfma_f32_16x16x32_bf16 v[104:107], v[152:155], v[190:193], v[104:107]
	v_mfma_f32_16x16x32_bf16 v[96:99], v[160:163], v[190:193], v[96:99]
	v_mfma_f32_16x16x32_bf16 v[88:91], v[152:155], v[198:201], v[88:91]
	v_mfma_f32_16x16x32_bf16 v[80:83], v[160:163], v[198:201], v[80:83]
	v_mfma_f32_16x16x32_bf16 v[72:75], v[152:155], v[206:209], v[72:75]
	v_mfma_f32_16x16x32_bf16 v[68:71], v[160:163], v[206:209], v[68:71]
	s_setprio 0
	s_barrier
	s_add_i32 s22, s59, s45
	v_lshl_add_u64 v[176:177], s[40:41], 0, v[2:3]
	s_mov_b32 m0, s22
	ds_read_b128 v[172:175], v181 offset:16384
	ds_read_b128 v[182:185], v181 offset:17408
	ds_read_b128 v[186:189], v181 offset:18432
	ds_read_b128 v[190:193], v181 offset:19456
	ds_read_b128 v[194:197], v181 offset:20480
	ds_read_b128 v[198:201], v181 offset:21504
	ds_read_b128 v[202:205], v181 offset:22528
	ds_read_b128 v[206:209], v181 offset:23552
	global_load_lds_dwordx4 v[176:177], off
	s_add_i32 m0, s22, 0x2000
	s_add_u32 s22, s40, 0x40000
	v_lshl_add_u64 v[210:211], s[40:41], 0, v[166:167]
	s_addc_u32 s23, s41, 0
	s_add_i32 s59, s60, s45
	global_load_lds_dwordx4 v[210:211], off
	v_lshl_add_u64 v[212:213], s[22:23], 0, v[2:3]
	s_mov_b32 m0, s59
	v_lshl_add_u64 v[214:215], s[42:43], 0, v[164:165]
	global_load_lds_dwordx4 v[212:213], off
	v_lshl_add_u64 v[212:213], s[22:23], 0, v[166:167]
	s_add_i32 m0, s59, 0x2000
	s_nop 0
	global_load_lds_dwordx4 v[212:213], off
	v_lshl_add_u64 v[212:213], s[42:43], 0, v[0:1]
	s_mov_b32 m0, s46
	s_nop 0
	global_load_lds_dwordx4 v[212:213], off
	s_mov_b32 m0, s47
	s_nop 0
	global_load_lds_dwordx4 v[214:215], off
	s_waitcnt vmcnt(8)
	s_waitcnt lgkmcnt(0)
	s_barrier
	s_setprio 1
	s_waitcnt lgkmcnt(0)
	v_mfma_f32_16x16x32_bf16 v[64:67], v[116:119], v[172:175], 0
	v_mfma_f32_16x16x32_bf16 v[60:63], v[124:127], v[172:175], 0
	v_mfma_f32_16x16x32_bf16 v[48:51], v[116:119], v[186:189], 0
	v_mfma_f32_16x16x32_bf16 v[44:47], v[124:127], v[186:189], 0
	v_mfma_f32_16x16x32_bf16 v[36:39], v[116:119], v[194:197], 0
	v_mfma_f32_16x16x32_bf16 v[28:31], v[124:127], v[194:197], 0
	v_mfma_f32_16x16x32_bf16 v[20:23], v[116:119], v[202:205], 0
	v_mfma_f32_16x16x32_bf16 v[12:15], v[124:127], v[202:205], 0
	v_mfma_f32_16x16x32_bf16 v[64:67], v[120:123], v[182:185], v[64:67]
	v_mfma_f32_16x16x32_bf16 v[60:63], v[128:131], v[182:185], v[60:63]
	v_mfma_f32_16x16x32_bf16 v[48:51], v[120:123], v[190:193], v[48:51]
	v_mfma_f32_16x16x32_bf16 v[44:47], v[128:131], v[190:193], v[44:47]
	v_mfma_f32_16x16x32_bf16 v[36:39], v[120:123], v[198:201], v[36:39]
	v_mfma_f32_16x16x32_bf16 v[28:31], v[128:131], v[198:201], v[28:31]
	v_mfma_f32_16x16x32_bf16 v[20:23], v[120:123], v[206:209], v[20:23]
	v_mfma_f32_16x16x32_bf16 v[12:15], v[128:131], v[206:209], v[12:15]
	s_setprio 0
	s_setprio 1
	v_mfma_f32_16x16x32_bf16 v[56:59], v[148:151], v[172:175], 0
	v_mfma_f32_16x16x32_bf16 v[52:55], v[156:159], v[172:175], 0
	v_mfma_f32_16x16x32_bf16 v[40:43], v[148:151], v[186:189], 0
	v_mfma_f32_16x16x32_bf16 v[32:35], v[156:159], v[186:189], 0
	v_mfma_f32_16x16x32_bf16 v[24:27], v[148:151], v[194:197], 0
	v_mfma_f32_16x16x32_bf16 v[16:19], v[156:159], v[194:197], 0
	v_mfma_f32_16x16x32_bf16 v[8:11], v[148:151], v[202:205], 0
	v_mfma_f32_16x16x32_bf16 v[4:7], v[156:159], v[202:205], 0
	v_mfma_f32_16x16x32_bf16 v[56:59], v[152:155], v[182:185], v[56:59]
	v_mfma_f32_16x16x32_bf16 v[52:55], v[160:163], v[182:185], v[52:55]
	v_mfma_f32_16x16x32_bf16 v[40:43], v[152:155], v[190:193], v[40:43]
	v_mfma_f32_16x16x32_bf16 v[32:35], v[160:163], v[190:193], v[32:35]
	v_mfma_f32_16x16x32_bf16 v[24:27], v[152:155], v[198:201], v[24:27]
	v_mfma_f32_16x16x32_bf16 v[16:19], v[160:163], v[198:201], v[16:19]
	v_mfma_f32_16x16x32_bf16 v[8:11], v[152:155], v[206:209], v[8:11]
	v_mfma_f32_16x16x32_bf16 v[4:7], v[160:163], v[206:209], v[4:7]
	s_setprio 0
	s_barrier
	s_add_i32 s59, 0, 0x18000
	s_add_i32 s60, 0, 0x1c000
	v_add_u32_e32 v128, s59, v179
	v_add_u32_e32 v160, s60, v179
	ds_read_b128 v[116:119], v128
	ds_read_b128 v[120:123], v128 offset:1024
	ds_read_b128 v[124:127], v128 offset:2048
	ds_read_b128 v[128:131], v128 offset:3072
	ds_read_b128 v[148:151], v160
	ds_read_b128 v[152:155], v160 offset:1024
	ds_read_b128 v[156:159], v160 offset:2048
	ds_read_b128 v[160:163], v160 offset:3072
	s_add_u32 s22, s42, 0x40000
	s_addc_u32 s23, s43, 0
	s_mov_b32 m0, s52
	v_lshl_add_u64 v[216:217], s[22:23], 0, v[0:1]
	ds_read_b128 v[172:175], v181 offset:32768
	ds_read_b128 v[182:185], v181 offset:33792
	ds_read_b128 v[186:189], v181 offset:34816
	ds_read_b128 v[190:193], v181 offset:35840
	ds_read_b128 v[194:197], v181 offset:36864
	ds_read_b128 v[198:201], v181 offset:37888
	ds_read_b128 v[202:205], v181 offset:38912
	ds_read_b128 v[206:209], v181 offset:39936
	global_load_lds_dwordx4 v[216:217], off
	v_lshl_add_u64 v[216:217], s[22:23], 0, v[164:165]
	s_mov_b32 m0, s53
	s_nop 0
	global_load_lds_dwordx4 v[216:217], off
	s_waitcnt vmcnt(8)
	s_waitcnt lgkmcnt(0)
	s_barrier
	s_setprio 1
	s_waitcnt lgkmcnt(0)
	v_mfma_f32_16x16x32_bf16 v[144:147], v[116:119], v[172:175], v[144:147]
	v_mfma_f32_16x16x32_bf16 v[140:143], v[124:127], v[172:175], v[140:143]
	v_mfma_f32_16x16x32_bf16 v[112:115], v[116:119], v[186:189], v[112:115]
	v_mfma_f32_16x16x32_bf16 v[108:111], v[124:127], v[186:189], v[108:111]
	v_mfma_f32_16x16x32_bf16 v[100:103], v[116:119], v[194:197], v[100:103]
	v_mfma_f32_16x16x32_bf16 v[92:95], v[124:127], v[194:197], v[92:95]
	v_mfma_f32_16x16x32_bf16 v[84:87], v[116:119], v[202:205], v[84:87]
	v_mfma_f32_16x16x32_bf16 v[76:79], v[124:127], v[202:205], v[76:79]
	v_mfma_f32_16x16x32_bf16 v[144:147], v[120:123], v[182:185], v[144:147]
	v_mfma_f32_16x16x32_bf16 v[140:143], v[128:131], v[182:185], v[140:143]
	v_mfma_f32_16x16x32_bf16 v[112:115], v[120:123], v[190:193], v[112:115]
	v_mfma_f32_16x16x32_bf16 v[108:111], v[128:131], v[190:193], v[108:111]
	v_mfma_f32_16x16x32_bf16 v[100:103], v[120:123], v[198:201], v[100:103]
	v_mfma_f32_16x16x32_bf16 v[92:95], v[128:131], v[198:201], v[92:95]
	v_mfma_f32_16x16x32_bf16 v[84:87], v[120:123], v[206:209], v[84:87]
	v_mfma_f32_16x16x32_bf16 v[76:79], v[128:131], v[206:209], v[76:79]
	s_setprio 0
	s_setprio 1
	v_mfma_f32_16x16x32_bf16 v[136:139], v[148:151], v[172:175], v[136:139]
	v_mfma_f32_16x16x32_bf16 v[132:135], v[156:159], v[172:175], v[132:135]
	v_mfma_f32_16x16x32_bf16 v[104:107], v[148:151], v[186:189], v[104:107]
	v_mfma_f32_16x16x32_bf16 v[96:99], v[156:159], v[186:189], v[96:99]
	v_mfma_f32_16x16x32_bf16 v[88:91], v[148:151], v[194:197], v[88:91]
	v_mfma_f32_16x16x32_bf16 v[80:83], v[156:159], v[194:197], v[80:83]
	v_mfma_f32_16x16x32_bf16 v[72:75], v[148:151], v[202:205], v[72:75]
	v_mfma_f32_16x16x32_bf16 v[68:71], v[156:159], v[202:205], v[68:71]
	v_mfma_f32_16x16x32_bf16 v[136:139], v[152:155], v[182:185], v[136:139]
	v_mfma_f32_16x16x32_bf16 v[132:135], v[160:163], v[182:185], v[132:135]
	v_mfma_f32_16x16x32_bf16 v[104:107], v[152:155], v[190:193], v[104:107]
	v_mfma_f32_16x16x32_bf16 v[96:99], v[160:163], v[190:193], v[96:99]
	v_mfma_f32_16x16x32_bf16 v[88:91], v[152:155], v[198:201], v[88:91]
	v_mfma_f32_16x16x32_bf16 v[80:83], v[160:163], v[198:201], v[80:83]
	v_mfma_f32_16x16x32_bf16 v[72:75], v[152:155], v[206:209], v[72:75]
	v_mfma_f32_16x16x32_bf16 v[68:71], v[160:163], v[206:209], v[68:71]
	s_setprio 0
	s_barrier
	s_add_i32 s22, s59, s45
	v_lshl_add_u64 v[176:177], v[176:177], 0, s[28:29]
	s_mov_b32 m0, s22
	ds_read_b128 v[172:175], v181 offset:49152
	ds_read_b128 v[182:185], v181 offset:50176
	ds_read_b128 v[186:189], v181 offset:51200
	ds_read_b128 v[190:193], v181 offset:52224
	ds_read_b128 v[194:197], v181 offset:53248
	ds_read_b128 v[198:201], v181 offset:54272
	ds_read_b128 v[202:205], v181 offset:55296
	ds_read_b128 v[206:209], v181 offset:56320
	global_load_lds_dwordx4 v[176:177], off
	s_add_i32 m0, s22, 0x2000
	s_add_u32 s22, s40, 0x40080
	v_lshl_add_u64 v[176:177], v[210:211], 0, s[28:29]
	s_addc_u32 s23, s41, 0
	s_add_i32 s40, s60, s45
	global_load_lds_dwordx4 v[176:177], off
	v_lshl_add_u64 v[176:177], s[22:23], 0, v[2:3]
	s_mov_b32 m0, s40
	s_nop 0
	global_load_lds_dwordx4 v[176:177], off
	v_lshl_add_u64 v[176:177], s[22:23], 0, v[166:167]
	s_add_i32 m0, s40, 0x2000
	s_nop 0
	global_load_lds_dwordx4 v[176:177], off
	v_lshl_add_u64 v[176:177], v[212:213], 0, s[28:29]
	s_mov_b32 m0, s55
	s_nop 0
	global_load_lds_dwordx4 v[176:177], off
	v_lshl_add_u64 v[176:177], v[214:215], 0, s[28:29]
	s_mov_b32 m0, s56
	s_nop 0
	global_load_lds_dwordx4 v[176:177], off
	s_waitcnt vmcnt(8)
	s_waitcnt lgkmcnt(0)
	s_barrier
	s_setprio 1
	s_waitcnt lgkmcnt(0)
	v_mfma_f32_16x16x32_bf16 v[64:67], v[116:119], v[172:175], v[64:67]
	v_mfma_f32_16x16x32_bf16 v[60:63], v[124:127], v[172:175], v[60:63]
	v_mfma_f32_16x16x32_bf16 v[48:51], v[116:119], v[186:189], v[48:51]
	v_mfma_f32_16x16x32_bf16 v[44:47], v[124:127], v[186:189], v[44:47]
	v_mfma_f32_16x16x32_bf16 v[36:39], v[116:119], v[194:197], v[36:39]
	v_mfma_f32_16x16x32_bf16 v[28:31], v[124:127], v[194:197], v[28:31]
	v_mfma_f32_16x16x32_bf16 v[20:23], v[116:119], v[202:205], v[20:23]
	v_mfma_f32_16x16x32_bf16 v[12:15], v[124:127], v[202:205], v[12:15]
	v_mfma_f32_16x16x32_bf16 v[64:67], v[120:123], v[182:185], v[64:67]
	v_mfma_f32_16x16x32_bf16 v[60:63], v[128:131], v[182:185], v[60:63]
	v_mfma_f32_16x16x32_bf16 v[48:51], v[120:123], v[190:193], v[48:51]
	v_mfma_f32_16x16x32_bf16 v[44:47], v[128:131], v[190:193], v[44:47]
	v_mfma_f32_16x16x32_bf16 v[36:39], v[120:123], v[198:201], v[36:39]
	v_mfma_f32_16x16x32_bf16 v[28:31], v[128:131], v[198:201], v[28:31]
	v_mfma_f32_16x16x32_bf16 v[20:23], v[120:123], v[206:209], v[20:23]
	v_mfma_f32_16x16x32_bf16 v[12:15], v[128:131], v[206:209], v[12:15]
	s_setprio 0
	s_setprio 1
	v_mfma_f32_16x16x32_bf16 v[56:59], v[148:151], v[172:175], v[56:59]
	v_mfma_f32_16x16x32_bf16 v[52:55], v[156:159], v[172:175], v[52:55]
	v_mfma_f32_16x16x32_bf16 v[40:43], v[148:151], v[186:189], v[40:43]
	v_mfma_f32_16x16x32_bf16 v[32:35], v[156:159], v[186:189], v[32:35]
	v_mfma_f32_16x16x32_bf16 v[24:27], v[148:151], v[194:197], v[24:27]
	v_mfma_f32_16x16x32_bf16 v[16:19], v[156:159], v[194:197], v[16:19]
	v_mfma_f32_16x16x32_bf16 v[8:11], v[148:151], v[202:205], v[8:11]
	v_mfma_f32_16x16x32_bf16 v[4:7], v[156:159], v[202:205], v[4:7]
	v_mfma_f32_16x16x32_bf16 v[56:59], v[152:155], v[182:185], v[56:59]
	v_mfma_f32_16x16x32_bf16 v[52:55], v[160:163], v[182:185], v[52:55]
	v_mfma_f32_16x16x32_bf16 v[40:43], v[152:155], v[190:193], v[40:43]
	v_mfma_f32_16x16x32_bf16 v[32:35], v[160:163], v[190:193], v[32:35]
	v_mfma_f32_16x16x32_bf16 v[24:27], v[152:155], v[198:201], v[24:27]
	v_mfma_f32_16x16x32_bf16 v[16:19], v[160:163], v[198:201], v[16:19]
	v_mfma_f32_16x16x32_bf16 v[8:11], v[152:155], v[206:209], v[8:11]
	v_mfma_f32_16x16x32_bf16 v[4:7], v[160:163], v[206:209], v[4:7]
	s_setprio 0
	s_barrier
	s_add_i32 s58, s58, 2
	s_add_u32 s13, s13, 0x100
	s_addc_u32 s15, s15, 0
	s_cmp_gt_u32 s58, 13
	s_mov_b64 s[22:23], s[26:27]
	s_cbranch_scc1 .Lmy_gx1

.LBB0_1035:
	s_ashr_i32 s15, s14, 31
	s_lshl_b64 s[18:19], s[14:15], 19
	s_add_u32 s18, s25, s18
	s_addc_u32 s19, s31, s19
	s_and_b64 s[20:21], s[38:39], exec
	s_cselect_b32 s15, s19, s23
	s_cselect_b32 s54, s18, s22
	s_ashr_i32 s13, s12, 31
	s_lshl_b64 s[20:21], s[12:13], 19
	s_add_u32 s20, s35, s20
	s_addc_u32 s21, s36, s21
	s_and_b64 s[40:41], s[38:39], exec
	s_cselect_b32 s13, s21, s27
	s_cselect_b32 s55, s20, s26
	s_add_u32 s56, s26, 0x100
	s_addc_u32 s57, s27, 0
	s_mov_b32 s58, -2
	s_add_u32 s26, s22, 0x100
	s_addc_u32 s27, s23, 0
	s_add_i32 s59, 0, 0x10000
	s_cmp_eq_u32 s58, 12
	s_cselect_b32 s43, s15, s27
	s_cselect_b32 s42, s54, s26
	s_cselect_b32 s41, s13, s57
	s_cselect_b32 s40, s55, s56
	s_add_i32 s60, 0, 0x14000
	v_add_u32_e32 v156, s59, v141
	v_add_u32_e32 v172, s60, v141
	ds_read_b128 v[144:147], v156
	ds_read_b128 v[148:151], v156 offset:1024
	ds_read_b128 v[152:155], v156 offset:2048
	ds_read_b128 v[156:159], v156 offset:3072
	ds_read_b128 v[160:163], v172
	ds_read_b128 v[164:167], v172 offset:1024
	ds_read_b128 v[168:171], v172 offset:2048
	ds_read_b128 v[172:175], v172 offset:3072
	v_lshl_add_u64 v[208:209], s[22:23], 0, v[138:139]
	s_add_i32 m0, s45, 0xc000
	ds_read_b128 v[176:179], v143
	ds_read_b128 v[180:183], v143 offset:1024
	ds_read_b128 v[184:187], v143 offset:2048
	ds_read_b128 v[188:191], v143 offset:3072
	ds_read_b128 v[192:195], v143 offset:4096
	ds_read_b128 v[196:199], v143 offset:5120
	ds_read_b128 v[200:203], v143 offset:6144
	ds_read_b128 v[204:207], v143 offset:7168
	global_load_lds_dwordx4 v[208:209], off
	v_lshl_add_u64 v[208:209], s[22:23], 0, v[136:137]
	s_add_i32 m0, s45, 0xe000
	s_nop 0
	global_load_lds_dwordx4 v[208:209], off
	s_waitcnt vmcnt(8)
	s_waitcnt lgkmcnt(0)
	s_barrier
	s_setprio 1
	s_waitcnt lgkmcnt(0)
	v_mfma_f32_16x16x32_bf16 v[128:131], v[144:147], v[176:179], 0
	v_mfma_f32_16x16x32_bf16 v[120:123], v[152:155], v[176:179], 0
	v_mfma_f32_16x16x32_bf16 v[112:115], v[144:147], v[184:187], 0
	v_mfma_f32_16x16x32_bf16 v[104:107], v[152:155], v[184:187], 0
	v_mfma_f32_16x16x32_bf16 v[96:99], v[144:147], v[192:195], 0
	v_mfma_f32_16x16x32_bf16 v[88:91], v[152:155], v[192:195], 0
	v_mfma_f32_16x16x32_bf16 v[80:83], v[144:147], v[200:203], 0
	v_mfma_f32_16x16x32_bf16 v[72:75], v[152:155], v[200:203], 0
	v_mfma_f32_16x16x32_bf16 v[128:131], v[148:151], v[180:183], v[128:131]
	v_mfma_f32_16x16x32_bf16 v[120:123], v[156:159], v[180:183], v[120:123]
	v_mfma_f32_16x16x32_bf16 v[112:115], v[148:151], v[188:191], v[112:115]
	v_mfma_f32_16x16x32_bf16 v[104:107], v[156:159], v[188:191], v[104:107]
	v_mfma_f32_16x16x32_bf16 v[96:99], v[148:151], v[196:199], v[96:99]
	v_mfma_f32_16x16x32_bf16 v[88:91], v[156:159], v[196:199], v[88:91]
	v_mfma_f32_16x16x32_bf16 v[80:83], v[148:151], v[204:207], v[80:83]
	v_mfma_f32_16x16x32_bf16 v[72:75], v[156:159], v[204:207], v[72:75]
	s_setprio 0
	s_setprio 1
	v_mfma_f32_16x16x32_bf16 v[124:127], v[160:163], v[176:179], 0
	v_mfma_f32_16x16x32_bf16 v[116:119], v[168:171], v[176:179], 0
	v_mfma_f32_16x16x32_bf16 v[108:111], v[160:163], v[184:187], 0
	v_mfma_f32_16x16x32_bf16 v[100:103], v[168:171], v[184:187], 0
	v_mfma_f32_16x16x32_bf16 v[92:95], v[160:163], v[192:195], 0
	v_mfma_f32_16x16x32_bf16 v[84:87], v[168:171], v[192:195], 0
	v_mfma_f32_16x16x32_bf16 v[76:79], v[160:163], v[200:203], 0
	v_mfma_f32_16x16x32_bf16 v[68:71], v[168:171], v[200:203], 0
	v_mfma_f32_16x16x32_bf16 v[124:127], v[164:167], v[180:183], v[124:127]
	v_mfma_f32_16x16x32_bf16 v[116:119], v[172:175], v[180:183], v[116:119]
	v_mfma_f32_16x16x32_bf16 v[108:111], v[164:167], v[188:191], v[108:111]
	v_mfma_f32_16x16x32_bf16 v[100:103], v[172:175], v[188:191], v[100:103]
	v_mfma_f32_16x16x32_bf16 v[92:95], v[164:167], v[196:199], v[92:95]
	v_mfma_f32_16x16x32_bf16 v[84:87], v[172:175], v[196:199], v[84:87]
	v_mfma_f32_16x16x32_bf16 v[76:79], v[164:167], v[204:207], v[76:79]
	v_mfma_f32_16x16x32_bf16 v[68:71], v[172:175], v[204:207], v[68:71]
	s_setprio 0
	s_barrier
	s_add_i32 s22, s59, s37
	v_lshl_add_u64 v[208:209], s[40:41], 0, v[2:3]
	s_mov_b32 m0, s22
	ds_read_b128 v[176:179], v143 offset:16384
	ds_read_b128 v[180:183], v143 offset:17408
	ds_read_b128 v[184:187], v143 offset:18432
	ds_read_b128 v[188:191], v143 offset:19456
	ds_read_b128 v[192:195], v143 offset:20480
	ds_read_b128 v[196:199], v143 offset:21504
	ds_read_b128 v[200:203], v143 offset:22528
	ds_read_b128 v[204:207], v143 offset:23552
	global_load_lds_dwordx4 v[208:209], off
	s_add_i32 m0, s22, 0x2000
	s_add_u32 s22, s40, 0x40000
	v_lshl_add_u64 v[210:211], s[40:41], 0, v[0:1]
	s_addc_u32 s23, s41, 0
	s_add_i32 s59, s60, s37
	global_load_lds_dwordx4 v[210:211], off
	v_lshl_add_u64 v[212:213], s[22:23], 0, v[2:3]
	s_mov_b32 m0, s59
	v_lshl_add_u64 v[214:215], s[42:43], 0, v[132:133]
	global_load_lds_dwordx4 v[212:213], off
	v_lshl_add_u64 v[212:213], s[22:23], 0, v[0:1]
	s_add_i32 m0, s59, 0x2000
	s_nop 0
	global_load_lds_dwordx4 v[212:213], off
	v_lshl_add_u64 v[212:213], s[42:43], 0, v[134:135]
	s_mov_b32 m0, s45
	s_nop 0
	global_load_lds_dwordx4 v[212:213], off
	s_mov_b32 m0, s46
	s_nop 0
	global_load_lds_dwordx4 v[214:215], off
	s_waitcnt vmcnt(8)
	s_waitcnt lgkmcnt(0)
	s_barrier
	s_setprio 1
	s_waitcnt lgkmcnt(0)
	v_mfma_f32_16x16x32_bf16 v[64:67], v[144:147], v[176:179], 0
	v_mfma_f32_16x16x32_bf16 v[56:59], v[152:155], v[176:179], 0
	v_mfma_f32_16x16x32_bf16 v[48:51], v[144:147], v[184:187], 0
	v_mfma_f32_16x16x32_bf16 v[40:43], v[152:155], v[184:187], 0
	v_mfma_f32_16x16x32_bf16 v[32:35], v[144:147], v[192:195], 0
	v_mfma_f32_16x16x32_bf16 v[24:27], v[152:155], v[192:195], 0
	v_mfma_f32_16x16x32_bf16 v[16:19], v[144:147], v[200:203], 0
	v_mfma_f32_16x16x32_bf16 v[8:11], v[152:155], v[200:203], 0
	v_mfma_f32_16x16x32_bf16 v[64:67], v[148:151], v[180:183], v[64:67]
	v_mfma_f32_16x16x32_bf16 v[56:59], v[156:159], v[180:183], v[56:59]
	v_mfma_f32_16x16x32_bf16 v[48:51], v[148:151], v[188:191], v[48:51]
	v_mfma_f32_16x16x32_bf16 v[40:43], v[156:159], v[188:191], v[40:43]
	v_mfma_f32_16x16x32_bf16 v[32:35], v[148:151], v[196:199], v[32:35]
	v_mfma_f32_16x16x32_bf16 v[24:27], v[156:159], v[196:199], v[24:27]
	v_mfma_f32_16x16x32_bf16 v[16:19], v[148:151], v[204:207], v[16:19]
	v_mfma_f32_16x16x32_bf16 v[8:11], v[156:159], v[204:207], v[8:11]
	s_setprio 0
	s_setprio 1
	v_mfma_f32_16x16x32_bf16 v[60:63], v[160:163], v[176:179], 0
	v_mfma_f32_16x16x32_bf16 v[52:55], v[168:171], v[176:179], 0
	v_mfma_f32_16x16x32_bf16 v[44:47], v[160:163], v[184:187], 0
	v_mfma_f32_16x16x32_bf16 v[36:39], v[168:171], v[184:187], 0
	v_mfma_f32_16x16x32_bf16 v[28:31], v[160:163], v[192:195], 0
	v_mfma_f32_16x16x32_bf16 v[20:23], v[168:171], v[192:195], 0
	v_mfma_f32_16x16x32_bf16 v[12:15], v[160:163], v[200:203], 0
	v_mfma_f32_16x16x32_bf16 v[4:7], v[168:171], v[200:203], 0
	v_mfma_f32_16x16x32_bf16 v[60:63], v[164:167], v[180:183], v[60:63]
	v_mfma_f32_16x16x32_bf16 v[52:55], v[172:175], v[180:183], v[52:55]
	v_mfma_f32_16x16x32_bf16 v[44:47], v[164:167], v[188:191], v[44:47]
	v_mfma_f32_16x16x32_bf16 v[36:39], v[172:175], v[188:191], v[36:39]
	v_mfma_f32_16x16x32_bf16 v[28:31], v[164:167], v[196:199], v[28:31]
	v_mfma_f32_16x16x32_bf16 v[20:23], v[172:175], v[196:199], v[20:23]
	v_mfma_f32_16x16x32_bf16 v[12:15], v[164:167], v[204:207], v[12:15]
	v_mfma_f32_16x16x32_bf16 v[4:7], v[172:175], v[204:207], v[4:7]
	s_setprio 0
	s_barrier
	s_add_i32 s59, 0, 0x18000
	s_add_i32 s60, 0, 0x1c000
	v_add_u32_e32 v156, s59, v141
	v_add_u32_e32 v172, s60, v141
	ds_read_b128 v[144:147], v156
	ds_read_b128 v[148:151], v156 offset:1024
	ds_read_b128 v[152:155], v156 offset:2048
	ds_read_b128 v[156:159], v156 offset:3072
	ds_read_b128 v[160:163], v172
	ds_read_b128 v[164:167], v172 offset:1024
	ds_read_b128 v[168:171], v172 offset:2048
	ds_read_b128 v[172:175], v172 offset:3072
	s_add_u32 s22, s42, 0x40000
	s_addc_u32 s23, s43, 0
	s_mov_b32 m0, s47
	v_lshl_add_u64 v[216:217], s[22:23], 0, v[134:135]
	ds_read_b128 v[176:179], v143 offset:32768
	ds_read_b128 v[180:183], v143 offset:33792
	ds_read_b128 v[184:187], v143 offset:34816
	ds_read_b128 v[188:191], v143 offset:35840
	ds_read_b128 v[192:195], v143 offset:36864
	ds_read_b128 v[196:199], v143 offset:37888
	ds_read_b128 v[200:203], v143 offset:38912
	ds_read_b128 v[204:207], v143 offset:39936
	global_load_lds_dwordx4 v[216:217], off
	v_lshl_add_u64 v[216:217], s[22:23], 0, v[132:133]
	s_mov_b32 m0, s50
	s_nop 0
	global_load_lds_dwordx4 v[216:217], off
	s_waitcnt vmcnt(8)
	s_waitcnt lgkmcnt(0)
	s_barrier
	s_setprio 1
	s_waitcnt lgkmcnt(0)
	v_mfma_f32_16x16x32_bf16 v[128:131], v[144:147], v[176:179], v[128:131]
	v_mfma_f32_16x16x32_bf16 v[120:123], v[152:155], v[176:179], v[120:123]
	v_mfma_f32_16x16x32_bf16 v[112:115], v[144:147], v[184:187], v[112:115]
	v_mfma_f32_16x16x32_bf16 v[104:107], v[152:155], v[184:187], v[104:107]
	v_mfma_f32_16x16x32_bf16 v[96:99], v[144:147], v[192:195], v[96:99]
	v_mfma_f32_16x16x32_bf16 v[88:91], v[152:155], v[192:195], v[88:91]
	v_mfma_f32_16x16x32_bf16 v[80:83], v[144:147], v[200:203], v[80:83]
	v_mfma_f32_16x16x32_bf16 v[72:75], v[152:155], v[200:203], v[72:75]
	v_mfma_f32_16x16x32_bf16 v[128:131], v[148:151], v[180:183], v[128:131]
	v_mfma_f32_16x16x32_bf16 v[120:123], v[156:159], v[180:183], v[120:123]
	v_mfma_f32_16x16x32_bf16 v[112:115], v[148:151], v[188:191], v[112:115]
	v_mfma_f32_16x16x32_bf16 v[104:107], v[156:159], v[188:191], v[104:107]
	v_mfma_f32_16x16x32_bf16 v[96:99], v[148:151], v[196:199], v[96:99]
	v_mfma_f32_16x16x32_bf16 v[88:91], v[156:159], v[196:199], v[88:91]
	v_mfma_f32_16x16x32_bf16 v[80:83], v[148:151], v[204:207], v[80:83]
	v_mfma_f32_16x16x32_bf16 v[72:75], v[156:159], v[204:207], v[72:75]
	s_setprio 0
	s_setprio 1
	v_mfma_f32_16x16x32_bf16 v[124:127], v[160:163], v[176:179], v[124:127]
	v_mfma_f32_16x16x32_bf16 v[116:119], v[168:171], v[176:179], v[116:119]
	v_mfma_f32_16x16x32_bf16 v[108:111], v[160:163], v[184:187], v[108:111]
	v_mfma_f32_16x16x32_bf16 v[100:103], v[168:171], v[184:187], v[100:103]
	v_mfma_f32_16x16x32_bf16 v[92:95], v[160:163], v[192:195], v[92:95]
	v_mfma_f32_16x16x32_bf16 v[84:87], v[168:171], v[192:195], v[84:87]
	v_mfma_f32_16x16x32_bf16 v[76:79], v[160:163], v[200:203], v[76:79]
	v_mfma_f32_16x16x32_bf16 v[68:71], v[168:171], v[200:203], v[68:71]
	v_mfma_f32_16x16x32_bf16 v[124:127], v[164:167], v[180:183], v[124:127]
	v_mfma_f32_16x16x32_bf16 v[116:119], v[172:175], v[180:183], v[116:119]
	v_mfma_f32_16x16x32_bf16 v[108:111], v[164:167], v[188:191], v[108:111]
	v_mfma_f32_16x16x32_bf16 v[100:103], v[172:175], v[188:191], v[100:103]
	v_mfma_f32_16x16x32_bf16 v[92:95], v[164:167], v[196:199], v[92:95]
	v_mfma_f32_16x16x32_bf16 v[84:87], v[172:175], v[196:199], v[84:87]
	v_mfma_f32_16x16x32_bf16 v[76:79], v[164:167], v[204:207], v[76:79]
	v_mfma_f32_16x16x32_bf16 v[68:71], v[172:175], v[204:207], v[68:71]
	s_setprio 0
	s_barrier
	s_add_i32 s22, s59, s37
	v_lshl_add_u64 v[208:209], v[208:209], 0, s[28:29]
	s_mov_b32 m0, s22
	ds_read_b128 v[176:179], v143 offset:49152
	ds_read_b128 v[180:183], v143 offset:50176
	ds_read_b128 v[184:187], v143 offset:51200
	ds_read_b128 v[188:191], v143 offset:52224
	ds_read_b128 v[192:195], v143 offset:53248
	ds_read_b128 v[196:199], v143 offset:54272
	ds_read_b128 v[200:203], v143 offset:55296
	ds_read_b128 v[204:207], v143 offset:56320
	global_load_lds_dwordx4 v[208:209], off
	s_add_i32 m0, s22, 0x2000
	s_add_u32 s22, s40, 0x40080
	v_lshl_add_u64 v[208:209], v[210:211], 0, s[28:29]
	s_addc_u32 s23, s41, 0
	s_add_i32 s40, s60, s37
	global_load_lds_dwordx4 v[208:209], off
	v_lshl_add_u64 v[208:209], s[22:23], 0, v[2:3]
	s_mov_b32 m0, s40
	s_nop 0
	global_load_lds_dwordx4 v[208:209], off
	v_lshl_add_u64 v[208:209], s[22:23], 0, v[0:1]
	s_add_i32 m0, s40, 0x2000
	s_nop 0
	global_load_lds_dwordx4 v[208:209], off
	v_lshl_add_u64 v[208:209], v[212:213], 0, s[28:29]
	s_mov_b32 m0, s51
	s_nop 0
	global_load_lds_dwordx4 v[208:209], off
	v_lshl_add_u64 v[208:209], v[214:215], 0, s[28:29]
	s_mov_b32 m0, s52
	s_nop 0
	global_load_lds_dwordx4 v[208:209], off
	s_waitcnt vmcnt(8)
	s_waitcnt lgkmcnt(0)
	s_barrier
	s_setprio 1
	s_waitcnt lgkmcnt(0)
	v_mfma_f32_16x16x32_bf16 v[64:67], v[144:147], v[176:179], v[64:67]
	v_mfma_f32_16x16x32_bf16 v[56:59], v[152:155], v[176:179], v[56:59]
	v_mfma_f32_16x16x32_bf16 v[48:51], v[144:147], v[184:187], v[48:51]
	v_mfma_f32_16x16x32_bf16 v[40:43], v[152:155], v[184:187], v[40:43]
	v_mfma_f32_16x16x32_bf16 v[32:35], v[144:147], v[192:195], v[32:35]
	v_mfma_f32_16x16x32_bf16 v[24:27], v[152:155], v[192:195], v[24:27]
	v_mfma_f32_16x16x32_bf16 v[16:19], v[144:147], v[200:203], v[16:19]
	v_mfma_f32_16x16x32_bf16 v[8:11], v[152:155], v[200:203], v[8:11]
	v_mfma_f32_16x16x32_bf16 v[64:67], v[148:151], v[180:183], v[64:67]
	v_mfma_f32_16x16x32_bf16 v[56:59], v[156:159], v[180:183], v[56:59]
	v_mfma_f32_16x16x32_bf16 v[48:51], v[148:151], v[188:191], v[48:51]
	v_mfma_f32_16x16x32_bf16 v[40:43], v[156:159], v[188:191], v[40:43]
	v_mfma_f32_16x16x32_bf16 v[32:35], v[148:151], v[196:199], v[32:35]
	v_mfma_f32_16x16x32_bf16 v[24:27], v[156:159], v[196:199], v[24:27]
	v_mfma_f32_16x16x32_bf16 v[16:19], v[148:151], v[204:207], v[16:19]
	v_mfma_f32_16x16x32_bf16 v[8:11], v[156:159], v[204:207], v[8:11]
	s_setprio 0
	s_setprio 1
	v_mfma_f32_16x16x32_bf16 v[60:63], v[160:163], v[176:179], v[60:63]
	v_mfma_f32_16x16x32_bf16 v[52:55], v[168:171], v[176:179], v[52:55]
	v_mfma_f32_16x16x32_bf16 v[44:47], v[160:163], v[184:187], v[44:47]
	v_mfma_f32_16x16x32_bf16 v[36:39], v[168:171], v[184:187], v[36:39]
	v_mfma_f32_16x16x32_bf16 v[28:31], v[160:163], v[192:195], v[28:31]
	v_mfma_f32_16x16x32_bf16 v[20:23], v[168:171], v[192:195], v[20:23]
	v_mfma_f32_16x16x32_bf16 v[12:15], v[160:163], v[200:203], v[12:15]
	v_mfma_f32_16x16x32_bf16 v[4:7], v[168:171], v[200:203], v[4:7]
	v_mfma_f32_16x16x32_bf16 v[60:63], v[164:167], v[180:183], v[60:63]
	v_mfma_f32_16x16x32_bf16 v[52:55], v[172:175], v[180:183], v[52:55]
	v_mfma_f32_16x16x32_bf16 v[44:47], v[164:167], v[188:191], v[44:47]
	v_mfma_f32_16x16x32_bf16 v[36:39], v[172:175], v[188:191], v[36:39]
	v_mfma_f32_16x16x32_bf16 v[28:31], v[164:167], v[196:199], v[28:31]
	v_mfma_f32_16x16x32_bf16 v[20:23], v[172:175], v[196:199], v[20:23]
	v_mfma_f32_16x16x32_bf16 v[12:15], v[164:167], v[204:207], v[12:15]
	v_mfma_f32_16x16x32_bf16 v[4:7], v[172:175], v[204:207], v[4:7]
	s_setprio 0
	s_barrier
	s_add_i32 s58, s58, 2
	s_add_u32 s56, s56, 0x100
	s_addc_u32 s57, s57, 0
	s_cmp_gt_u32 s58, 13
	s_mov_b64 s[22:23], s[26:27]
	s_cbranch_scc1 .Lmy_gx2

.LBB0_1111:
	s_add_u32 s54, s18, 0x100
	s_addc_u32 s55, s19, 0
	s_mov_b32 s56, -2
	s_waitcnt vmcnt(0)
	s_add_u32 s18, s10, 0x100
	s_addc_u32 s19, s11, 0
	s_add_i32 s57, 0, 0x10000
	s_cmp_eq_u32 s56, 40
	s_cselect_b32 s23, s1, s19
	s_cselect_b32 s22, s0, s18
	s_cselect_b32 s21, s15, s55
	s_cselect_b32 s20, s14, s54
	s_add_i32 s58, 0, 0x14000
	v_add_u32_e32 v128, s57, v179
	v_add_u32_e32 v160, s58, v179
	ds_read_b128 v[116:119], v128
	ds_read_b128 v[120:123], v128 offset:1024
	ds_read_b128 v[124:127], v128 offset:2048
	ds_read_b128 v[128:131], v128 offset:3072
	ds_read_b128 v[148:151], v160
	ds_read_b128 v[152:155], v160 offset:1024
	ds_read_b128 v[156:159], v160 offset:2048
	ds_read_b128 v[160:163], v160 offset:3072
	v_lshl_add_u64 v[176:177], s[10:11], 0, v[170:171]
	s_add_i32 m0, s40, 0xc000
	ds_read_b128 v[172:175], v181
	ds_read_b128 v[182:185], v181 offset:1024
	ds_read_b128 v[186:189], v181 offset:2048
	ds_read_b128 v[190:193], v181 offset:3072
	ds_read_b128 v[194:197], v181 offset:4096
	ds_read_b128 v[198:201], v181 offset:5120
	ds_read_b128 v[202:205], v181 offset:6144
	ds_read_b128 v[206:209], v181 offset:7168
	global_load_lds_dwordx4 v[176:177], off
	v_lshl_add_u64 v[176:177], s[10:11], 0, v[168:169]
	s_add_i32 m0, s40, 0xe000
	s_nop 0
	global_load_lds_dwordx4 v[176:177], off
	s_waitcnt vmcnt(8)
	s_waitcnt lgkmcnt(0)
	s_barrier
	s_setprio 1
	s_waitcnt lgkmcnt(0)
	v_mfma_f32_16x16x32_bf16 v[144:147], v[116:119], v[172:175], 0
	v_mfma_f32_16x16x32_bf16 v[140:143], v[124:127], v[172:175], 0
	v_mfma_f32_16x16x32_bf16 v[112:115], v[116:119], v[186:189], 0
	v_mfma_f32_16x16x32_bf16 v[108:111], v[124:127], v[186:189], 0
	v_mfma_f32_16x16x32_bf16 v[100:103], v[116:119], v[194:197], 0
	v_mfma_f32_16x16x32_bf16 v[92:95], v[124:127], v[194:197], 0
	v_mfma_f32_16x16x32_bf16 v[84:87], v[116:119], v[202:205], 0
	v_mfma_f32_16x16x32_bf16 v[76:79], v[124:127], v[202:205], 0
	v_mfma_f32_16x16x32_bf16 v[144:147], v[120:123], v[182:185], v[144:147]
	v_mfma_f32_16x16x32_bf16 v[140:143], v[128:131], v[182:185], v[140:143]
	v_mfma_f32_16x16x32_bf16 v[112:115], v[120:123], v[190:193], v[112:115]
	v_mfma_f32_16x16x32_bf16 v[108:111], v[128:131], v[190:193], v[108:111]
	v_mfma_f32_16x16x32_bf16 v[100:103], v[120:123], v[198:201], v[100:103]
	v_mfma_f32_16x16x32_bf16 v[92:95], v[128:131], v[198:201], v[92:95]
	v_mfma_f32_16x16x32_bf16 v[84:87], v[120:123], v[206:209], v[84:87]
	v_mfma_f32_16x16x32_bf16 v[76:79], v[128:131], v[206:209], v[76:79]
	s_setprio 0
	s_setprio 1
	v_mfma_f32_16x16x32_bf16 v[136:139], v[148:151], v[172:175], 0
	v_mfma_f32_16x16x32_bf16 v[132:135], v[156:159], v[172:175], 0
	v_mfma_f32_16x16x32_bf16 v[104:107], v[148:151], v[186:189], 0
	v_mfma_f32_16x16x32_bf16 v[96:99], v[156:159], v[186:189], 0
	v_mfma_f32_16x16x32_bf16 v[88:91], v[148:151], v[194:197], 0
	v_mfma_f32_16x16x32_bf16 v[80:83], v[156:159], v[194:197], 0
	v_mfma_f32_16x16x32_bf16 v[72:75], v[148:151], v[202:205], 0
	v_mfma_f32_16x16x32_bf16 v[68:71], v[156:159], v[202:205], 0
	v_mfma_f32_16x16x32_bf16 v[136:139], v[152:155], v[182:185], v[136:139]
	v_mfma_f32_16x16x32_bf16 v[132:135], v[160:163], v[182:185], v[132:135]
	v_mfma_f32_16x16x32_bf16 v[104:107], v[152:155], v[190:193], v[104:107]
	v_mfma_f32_16x16x32_bf16 v[96:99], v[160:163], v[190:193], v[96:99]
	v_mfma_f32_16x16x32_bf16 v[88:91], v[152:155], v[198:201], v[88:91]
	v_mfma_f32_16x16x32_bf16 v[80:83], v[160:163], v[198:201], v[80:83]
	v_mfma_f32_16x16x32_bf16 v[72:75], v[152:155], v[206:209], v[72:75]
	v_mfma_f32_16x16x32_bf16 v[68:71], v[160:163], v[206:209], v[68:71]
	s_setprio 0
	s_barrier
	s_add_i32 s10, s57, s37
	v_lshl_add_u64 v[176:177], s[20:21], 0, v[2:3]
	s_mov_b32 m0, s10
	ds_read_b128 v[172:175], v181 offset:16384
	ds_read_b128 v[182:185], v181 offset:17408
	ds_read_b128 v[186:189], v181 offset:18432
	ds_read_b128 v[190:193], v181 offset:19456
	ds_read_b128 v[194:197], v181 offset:20480
	ds_read_b128 v[198:201], v181 offset:21504
	ds_read_b128 v[202:205], v181 offset:22528
	ds_read_b128 v[206:209], v181 offset:23552
	global_load_lds_dwordx4 v[176:177], off
	s_add_i32 m0, s10, 0x2000
	s_add_u32 s10, s20, 0xb0000
	v_lshl_add_u64 v[210:211], s[20:21], 0, v[166:167]
	s_addc_u32 s11, s21, 0
	s_add_i32 s57, s58, s37
	global_load_lds_dwordx4 v[210:211], off
	v_lshl_add_u64 v[212:213], s[10:11], 0, v[2:3]
	s_mov_b32 m0, s57
	v_lshl_add_u64 v[214:215], s[22:23], 0, v[164:165]
	global_load_lds_dwordx4 v[212:213], off
	v_lshl_add_u64 v[212:213], s[10:11], 0, v[166:167]
	s_add_i32 m0, s57, 0x2000
	s_nop 0
	global_load_lds_dwordx4 v[212:213], off
	v_lshl_add_u64 v[212:213], s[22:23], 0, v[0:1]
	s_mov_b32 m0, s40
	s_nop 0
	global_load_lds_dwordx4 v[212:213], off
	s_mov_b32 m0, s41
	s_nop 0
	global_load_lds_dwordx4 v[214:215], off
	s_waitcnt vmcnt(8)
	s_waitcnt lgkmcnt(0)
	s_barrier
	s_setprio 1
	s_waitcnt lgkmcnt(0)
	v_mfma_f32_16x16x32_bf16 v[64:67], v[116:119], v[172:175], 0
	v_mfma_f32_16x16x32_bf16 v[60:63], v[124:127], v[172:175], 0
	v_mfma_f32_16x16x32_bf16 v[48:51], v[116:119], v[186:189], 0
	v_mfma_f32_16x16x32_bf16 v[44:47], v[124:127], v[186:189], 0
	v_mfma_f32_16x16x32_bf16 v[36:39], v[116:119], v[194:197], 0
	v_mfma_f32_16x16x32_bf16 v[28:31], v[124:127], v[194:197], 0
	v_mfma_f32_16x16x32_bf16 v[20:23], v[116:119], v[202:205], 0
	v_mfma_f32_16x16x32_bf16 v[12:15], v[124:127], v[202:205], 0
	v_mfma_f32_16x16x32_bf16 v[64:67], v[120:123], v[182:185], v[64:67]
	v_mfma_f32_16x16x32_bf16 v[60:63], v[128:131], v[182:185], v[60:63]
	v_mfma_f32_16x16x32_bf16 v[48:51], v[120:123], v[190:193], v[48:51]
	v_mfma_f32_16x16x32_bf16 v[44:47], v[128:131], v[190:193], v[44:47]
	v_mfma_f32_16x16x32_bf16 v[36:39], v[120:123], v[198:201], v[36:39]
	v_mfma_f32_16x16x32_bf16 v[28:31], v[128:131], v[198:201], v[28:31]
	v_mfma_f32_16x16x32_bf16 v[20:23], v[120:123], v[206:209], v[20:23]
	v_mfma_f32_16x16x32_bf16 v[12:15], v[128:131], v[206:209], v[12:15]
	s_setprio 0
	s_setprio 1
	v_mfma_f32_16x16x32_bf16 v[56:59], v[148:151], v[172:175], 0
	v_mfma_f32_16x16x32_bf16 v[52:55], v[156:159], v[172:175], 0
	v_mfma_f32_16x16x32_bf16 v[40:43], v[148:151], v[186:189], 0
	v_mfma_f32_16x16x32_bf16 v[32:35], v[156:159], v[186:189], 0
	v_mfma_f32_16x16x32_bf16 v[24:27], v[148:151], v[194:197], 0
	v_mfma_f32_16x16x32_bf16 v[16:19], v[156:159], v[194:197], 0
	v_mfma_f32_16x16x32_bf16 v[8:11], v[148:151], v[202:205], 0
	v_mfma_f32_16x16x32_bf16 v[4:7], v[156:159], v[202:205], 0
	v_mfma_f32_16x16x32_bf16 v[56:59], v[152:155], v[182:185], v[56:59]
	v_mfma_f32_16x16x32_bf16 v[52:55], v[160:163], v[182:185], v[52:55]
	v_mfma_f32_16x16x32_bf16 v[40:43], v[152:155], v[190:193], v[40:43]
	v_mfma_f32_16x16x32_bf16 v[32:35], v[160:163], v[190:193], v[32:35]
	v_mfma_f32_16x16x32_bf16 v[24:27], v[152:155], v[198:201], v[24:27]
	v_mfma_f32_16x16x32_bf16 v[16:19], v[160:163], v[198:201], v[16:19]
	v_mfma_f32_16x16x32_bf16 v[8:11], v[152:155], v[206:209], v[8:11]
	v_mfma_f32_16x16x32_bf16 v[4:7], v[160:163], v[206:209], v[4:7]
	s_setprio 0
	s_barrier
	s_add_i32 s57, 0, 0x18000
	s_add_i32 s58, 0, 0x1c000
	v_add_u32_e32 v128, s57, v179
	v_add_u32_e32 v160, s58, v179
	ds_read_b128 v[116:119], v128
	ds_read_b128 v[120:123], v128 offset:1024
	ds_read_b128 v[124:127], v128 offset:2048
	ds_read_b128 v[128:131], v128 offset:3072
	ds_read_b128 v[148:151], v160
	ds_read_b128 v[152:155], v160 offset:1024
	ds_read_b128 v[156:159], v160 offset:2048
	ds_read_b128 v[160:163], v160 offset:3072
	s_add_u32 s10, s22, 0xb0000
	s_addc_u32 s11, s23, 0
	s_mov_b32 m0, s42
	v_lshl_add_u64 v[216:217], s[10:11], 0, v[0:1]
	ds_read_b128 v[172:175], v181 offset:32768
	ds_read_b128 v[182:185], v181 offset:33792
	ds_read_b128 v[186:189], v181 offset:34816
	ds_read_b128 v[190:193], v181 offset:35840
	ds_read_b128 v[194:197], v181 offset:36864
	ds_read_b128 v[198:201], v181 offset:37888
	ds_read_b128 v[202:205], v181 offset:38912
	ds_read_b128 v[206:209], v181 offset:39936
	global_load_lds_dwordx4 v[216:217], off
	v_lshl_add_u64 v[216:217], s[10:11], 0, v[164:165]
	s_mov_b32 m0, s43
	s_nop 0
	global_load_lds_dwordx4 v[216:217], off
	s_waitcnt vmcnt(8)
	s_waitcnt lgkmcnt(0)
	s_barrier
	s_setprio 1
	s_waitcnt lgkmcnt(0)
	v_mfma_f32_16x16x32_bf16 v[144:147], v[116:119], v[172:175], v[144:147]
	v_mfma_f32_16x16x32_bf16 v[140:143], v[124:127], v[172:175], v[140:143]
	v_mfma_f32_16x16x32_bf16 v[112:115], v[116:119], v[186:189], v[112:115]
	v_mfma_f32_16x16x32_bf16 v[108:111], v[124:127], v[186:189], v[108:111]
	v_mfma_f32_16x16x32_bf16 v[100:103], v[116:119], v[194:197], v[100:103]
	v_mfma_f32_16x16x32_bf16 v[92:95], v[124:127], v[194:197], v[92:95]
	v_mfma_f32_16x16x32_bf16 v[84:87], v[116:119], v[202:205], v[84:87]
	v_mfma_f32_16x16x32_bf16 v[76:79], v[124:127], v[202:205], v[76:79]
	v_mfma_f32_16x16x32_bf16 v[144:147], v[120:123], v[182:185], v[144:147]
	v_mfma_f32_16x16x32_bf16 v[140:143], v[128:131], v[182:185], v[140:143]
	v_mfma_f32_16x16x32_bf16 v[112:115], v[120:123], v[190:193], v[112:115]
	v_mfma_f32_16x16x32_bf16 v[108:111], v[128:131], v[190:193], v[108:111]
	v_mfma_f32_16x16x32_bf16 v[100:103], v[120:123], v[198:201], v[100:103]
	v_mfma_f32_16x16x32_bf16 v[92:95], v[128:131], v[198:201], v[92:95]
	v_mfma_f32_16x16x32_bf16 v[84:87], v[120:123], v[206:209], v[84:87]
	v_mfma_f32_16x16x32_bf16 v[76:79], v[128:131], v[206:209], v[76:79]
	s_setprio 0
	s_setprio 1
	v_mfma_f32_16x16x32_bf16 v[136:139], v[148:151], v[172:175], v[136:139]
	v_mfma_f32_16x16x32_bf16 v[132:135], v[156:159], v[172:175], v[132:135]
	v_mfma_f32_16x16x32_bf16 v[104:107], v[148:151], v[186:189], v[104:107]
	v_mfma_f32_16x16x32_bf16 v[96:99], v[156:159], v[186:189], v[96:99]
	v_mfma_f32_16x16x32_bf16 v[88:91], v[148:151], v[194:197], v[88:91]
	v_mfma_f32_16x16x32_bf16 v[80:83], v[156:159], v[194:197], v[80:83]
	v_mfma_f32_16x16x32_bf16 v[72:75], v[148:151], v[202:205], v[72:75]
	v_mfma_f32_16x16x32_bf16 v[68:71], v[156:159], v[202:205], v[68:71]
	v_mfma_f32_16x16x32_bf16 v[136:139], v[152:155], v[182:185], v[136:139]
	v_mfma_f32_16x16x32_bf16 v[132:135], v[160:163], v[182:185], v[132:135]
	v_mfma_f32_16x16x32_bf16 v[104:107], v[152:155], v[190:193], v[104:107]
	v_mfma_f32_16x16x32_bf16 v[96:99], v[160:163], v[190:193], v[96:99]
	v_mfma_f32_16x16x32_bf16 v[88:91], v[152:155], v[198:201], v[88:91]
	v_mfma_f32_16x16x32_bf16 v[80:83], v[160:163], v[198:201], v[80:83]
	v_mfma_f32_16x16x32_bf16 v[72:75], v[152:155], v[206:209], v[72:75]
	v_mfma_f32_16x16x32_bf16 v[68:71], v[160:163], v[206:209], v[68:71]
	s_setprio 0
	s_barrier
	s_add_i32 s10, s57, s37
	v_lshl_add_u64 v[176:177], v[176:177], 0, s[28:29]
	s_mov_b32 m0, s10
	ds_read_b128 v[172:175], v181 offset:49152
	ds_read_b128 v[182:185], v181 offset:50176
	ds_read_b128 v[186:189], v181 offset:51200
	ds_read_b128 v[190:193], v181 offset:52224
	ds_read_b128 v[194:197], v181 offset:53248
	ds_read_b128 v[198:201], v181 offset:54272
	ds_read_b128 v[202:205], v181 offset:55296
	ds_read_b128 v[206:209], v181 offset:56320
	global_load_lds_dwordx4 v[176:177], off
	s_add_i32 m0, s10, 0x2000
	s_add_u32 s10, s20, 0xb0080
	v_lshl_add_u64 v[176:177], v[210:211], 0, s[28:29]
	s_addc_u32 s11, s21, 0
	s_add_i32 s20, s58, s37
	global_load_lds_dwordx4 v[176:177], off
	v_lshl_add_u64 v[176:177], s[10:11], 0, v[2:3]
	s_mov_b32 m0, s20
	s_nop 0
	global_load_lds_dwordx4 v[176:177], off
	v_lshl_add_u64 v[176:177], s[10:11], 0, v[166:167]
	s_add_i32 m0, s20, 0x2000
	s_nop 0
	global_load_lds_dwordx4 v[176:177], off
	v_lshl_add_u64 v[176:177], v[212:213], 0, s[28:29]
	s_mov_b32 m0, s45
	s_nop 0
	global_load_lds_dwordx4 v[176:177], off
	v_lshl_add_u64 v[176:177], v[214:215], 0, s[28:29]
	s_mov_b32 m0, s46
	s_nop 0
	global_load_lds_dwordx4 v[176:177], off
	s_waitcnt vmcnt(8)
	s_waitcnt lgkmcnt(0)
	s_barrier
	s_setprio 1
	s_waitcnt lgkmcnt(0)
	v_mfma_f32_16x16x32_bf16 v[64:67], v[116:119], v[172:175], v[64:67]
	v_mfma_f32_16x16x32_bf16 v[60:63], v[124:127], v[172:175], v[60:63]
	v_mfma_f32_16x16x32_bf16 v[48:51], v[116:119], v[186:189], v[48:51]
	v_mfma_f32_16x16x32_bf16 v[44:47], v[124:127], v[186:189], v[44:47]
	v_mfma_f32_16x16x32_bf16 v[36:39], v[116:119], v[194:197], v[36:39]
	v_mfma_f32_16x16x32_bf16 v[28:31], v[124:127], v[194:197], v[28:31]
	v_mfma_f32_16x16x32_bf16 v[20:23], v[116:119], v[202:205], v[20:23]
	v_mfma_f32_16x16x32_bf16 v[12:15], v[124:127], v[202:205], v[12:15]
	v_mfma_f32_16x16x32_bf16 v[64:67], v[120:123], v[182:185], v[64:67]
	v_mfma_f32_16x16x32_bf16 v[60:63], v[128:131], v[182:185], v[60:63]
	v_mfma_f32_16x16x32_bf16 v[48:51], v[120:123], v[190:193], v[48:51]
	v_mfma_f32_16x16x32_bf16 v[44:47], v[128:131], v[190:193], v[44:47]
	v_mfma_f32_16x16x32_bf16 v[36:39], v[120:123], v[198:201], v[36:39]
	v_mfma_f32_16x16x32_bf16 v[28:31], v[128:131], v[198:201], v[28:31]
	v_mfma_f32_16x16x32_bf16 v[20:23], v[120:123], v[206:209], v[20:23]
	v_mfma_f32_16x16x32_bf16 v[12:15], v[128:131], v[206:209], v[12:15]
	s_setprio 0
	s_setprio 1
	v_mfma_f32_16x16x32_bf16 v[56:59], v[148:151], v[172:175], v[56:59]
	v_mfma_f32_16x16x32_bf16 v[52:55], v[156:159], v[172:175], v[52:55]
	v_mfma_f32_16x16x32_bf16 v[40:43], v[148:151], v[186:189], v[40:43]
	v_mfma_f32_16x16x32_bf16 v[32:35], v[156:159], v[186:189], v[32:35]
	v_mfma_f32_16x16x32_bf16 v[24:27], v[148:151], v[194:197], v[24:27]
	v_mfma_f32_16x16x32_bf16 v[16:19], v[156:159], v[194:197], v[16:19]
	v_mfma_f32_16x16x32_bf16 v[8:11], v[148:151], v[202:205], v[8:11]
	v_mfma_f32_16x16x32_bf16 v[4:7], v[156:159], v[202:205], v[4:7]
	v_mfma_f32_16x16x32_bf16 v[56:59], v[152:155], v[182:185], v[56:59]
	v_mfma_f32_16x16x32_bf16 v[52:55], v[160:163], v[182:185], v[52:55]
	v_mfma_f32_16x16x32_bf16 v[40:43], v[152:155], v[190:193], v[40:43]
	v_mfma_f32_16x16x32_bf16 v[32:35], v[160:163], v[190:193], v[32:35]
	v_mfma_f32_16x16x32_bf16 v[24:27], v[152:155], v[198:201], v[24:27]
	v_mfma_f32_16x16x32_bf16 v[16:19], v[160:163], v[198:201], v[16:19]
	v_mfma_f32_16x16x32_bf16 v[8:11], v[152:155], v[206:209], v[8:11]
	v_mfma_f32_16x16x32_bf16 v[4:7], v[160:163], v[206:209], v[4:7]
	s_setprio 0
	s_barrier
	s_add_i32 s56, s56, 2
	s_add_u32 s54, s54, 0x100
	s_addc_u32 s55, s55, 0
	s_cmp_gt_u32 s56, 41
	s_mov_b64 s[10:11], s[18:19]
	s_cbranch_scc1 .Lmy_gx3

.Lmy_gx3:
	s_and_b64 vcc, exec, s[12:13]
	s_cbranch_vccz .LBB0_1115
	s_barrier

.LBB0_1329:
	s_ashr_i32 s17, s16, 31
	s_lshl_b64 s[18:19], s[16:17], 19
	s_add_u32 s18, s35, s18
	s_addc_u32 s19, s36, s19
	s_and_b64 s[20:21], s[38:39], exec
	s_cselect_b32 s13, s19, s23
	s_cselect_b32 s17, s18, s22
	s_ashr_i32 s15, s14, 31
	s_lshl_b64 s[20:21], s[14:15], 19
	s_add_u32 s20, s37, s20
	s_addc_u32 s21, s46, s21
	s_and_b64 s[40:41], s[38:39], exec
	s_cselect_b32 s15, s21, s27
	s_cselect_b32 s58, s20, s26
	s_add_u32 s59, s26, 0x100
	s_addc_u32 s60, s27, 0
	s_mov_b32 s61, -2
	s_add_u32 s26, s22, 0x100
	s_addc_u32 s27, s23, 0
	s_add_i32 s62, 0, 0x10000
	s_cmp_eq_u32 s61, 12
	s_cselect_b32 s43, s13, s27
	s_cselect_b32 s42, s17, s26
	v_add_u32_e32 v142, s62, v145
	s_cselect_b32 s41, s15, s60
	s_cselect_b32 s40, s58, s59
	s_add_i32 s63, 0, 0x14000
	ds_read_b128 v[148:151], v142
	ds_read_b128 v[152:155], v142 offset:1024
	ds_read_b128 v[156:159], v142 offset:2048
	ds_read_b128 v[160:163], v142 offset:3072
	v_add_u32_e32 v142, s63, v145
	ds_read_b128 v[164:167], v142
	ds_read_b128 v[168:171], v142 offset:1024
	ds_read_b128 v[172:175], v142 offset:2048
	ds_read_b128 v[176:179], v142 offset:3072
	v_lshl_add_u64 v[142:143], s[22:23], 0, v[140:141]
	s_add_i32 m0, s50, 0xc000
	ds_read_b128 v[180:183], v147
	ds_read_b128 v[184:187], v147 offset:1024
	ds_read_b128 v[188:191], v147 offset:2048
	ds_read_b128 v[192:195], v147 offset:3072
	ds_read_b128 v[196:199], v147 offset:4096
	ds_read_b128 v[200:203], v147 offset:5120
	ds_read_b128 v[204:207], v147 offset:6144
	ds_read_b128 v[208:211], v147 offset:7168
	global_load_lds_dwordx4 v[142:143], off
	v_lshl_add_u64 v[142:143], s[22:23], 0, v[138:139]
	s_add_i32 m0, s50, 0xe000
	s_nop 0
	global_load_lds_dwordx4 v[142:143], off
	s_waitcnt vmcnt(8)
	s_waitcnt lgkmcnt(0)
	s_barrier
	s_setprio 1
	s_waitcnt lgkmcnt(0)
	v_mfma_f32_16x16x32_bf16 v[96:99], v[148:151], v[180:183], 0
	v_mfma_f32_16x16x32_bf16 v[88:91], v[156:159], v[180:183], 0
	v_mfma_f32_16x16x32_bf16 v[80:83], v[148:151], v[188:191], 0
	v_mfma_f32_16x16x32_bf16 v[76:79], v[156:159], v[188:191], 0
	v_mfma_f32_16x16x32_bf16 v[72:75], v[148:151], v[196:199], 0
	v_mfma_f32_16x16x32_bf16 v[64:67], v[156:159], v[196:199], 0
	v_mfma_f32_16x16x32_bf16 v[56:59], v[148:151], v[204:207], 0
	v_mfma_f32_16x16x32_bf16 v[52:55], v[156:159], v[204:207], 0
	v_mfma_f32_16x16x32_bf16 v[96:99], v[152:155], v[184:187], v[96:99]
	v_mfma_f32_16x16x32_bf16 v[88:91], v[160:163], v[184:187], v[88:91]
	v_mfma_f32_16x16x32_bf16 v[80:83], v[152:155], v[192:195], v[80:83]
	v_mfma_f32_16x16x32_bf16 v[76:79], v[160:163], v[192:195], v[76:79]
	v_mfma_f32_16x16x32_bf16 v[72:75], v[152:155], v[200:203], v[72:75]
	v_mfma_f32_16x16x32_bf16 v[64:67], v[160:163], v[200:203], v[64:67]
	v_mfma_f32_16x16x32_bf16 v[56:59], v[152:155], v[208:211], v[56:59]
	v_mfma_f32_16x16x32_bf16 v[52:55], v[160:163], v[208:211], v[52:55]
	s_setprio 0
	s_setprio 1
	v_mfma_f32_16x16x32_bf16 v[128:131], v[164:167], v[180:183], 0
	v_mfma_f32_16x16x32_bf16 v[124:127], v[172:175], v[180:183], 0
	v_mfma_f32_16x16x32_bf16 v[120:123], v[164:167], v[188:191], 0
	v_mfma_f32_16x16x32_bf16 v[116:119], v[172:175], v[188:191], 0
	v_mfma_f32_16x16x32_bf16 v[112:115], v[164:167], v[196:199], 0
	v_mfma_f32_16x16x32_bf16 v[108:111], v[172:175], v[196:199], 0
	v_mfma_f32_16x16x32_bf16 v[104:107], v[164:167], v[204:207], 0
	v_mfma_f32_16x16x32_bf16 v[100:103], v[172:175], v[204:207], 0
	v_mfma_f32_16x16x32_bf16 v[128:131], v[168:171], v[184:187], v[128:131]
	v_mfma_f32_16x16x32_bf16 v[124:127], v[176:179], v[184:187], v[124:127]
	v_mfma_f32_16x16x32_bf16 v[120:123], v[168:171], v[192:195], v[120:123]
	v_mfma_f32_16x16x32_bf16 v[116:119], v[176:179], v[192:195], v[116:119]
	v_mfma_f32_16x16x32_bf16 v[112:115], v[168:171], v[200:203], v[112:115]
	v_mfma_f32_16x16x32_bf16 v[108:111], v[176:179], v[200:203], v[108:111]
	v_mfma_f32_16x16x32_bf16 v[104:107], v[168:171], v[208:211], v[104:107]
	v_mfma_f32_16x16x32_bf16 v[100:103], v[176:179], v[208:211], v[100:103]
	s_setprio 0
	s_barrier
	s_add_i32 s22, s62, s47
	v_lshl_add_u64 v[142:143], s[40:41], 0, v[2:3]
	s_mov_b32 m0, s22
	ds_read_b128 v[180:183], v147 offset:16384
	ds_read_b128 v[184:187], v147 offset:17408
	ds_read_b128 v[188:191], v147 offset:18432
	ds_read_b128 v[192:195], v147 offset:19456
	ds_read_b128 v[196:199], v147 offset:20480
	ds_read_b128 v[200:203], v147 offset:21504
	ds_read_b128 v[204:207], v147 offset:22528
	ds_read_b128 v[208:211], v147 offset:23552
	global_load_lds_dwordx4 v[142:143], off
	s_add_i32 m0, s22, 0x2000
	s_add_u32 s22, s40, 0x40000
	v_lshl_add_u64 v[212:213], s[40:41], 0, v[134:135]
	s_addc_u32 s23, s41, 0
	s_add_i32 s62, s63, s47
	global_load_lds_dwordx4 v[212:213], off
	v_lshl_add_u64 v[214:215], s[22:23], 0, v[2:3]
	s_mov_b32 m0, s62
	v_lshl_add_u64 v[216:217], s[42:43], 0, v[132:133]
	global_load_lds_dwordx4 v[214:215], off
	v_lshl_add_u64 v[214:215], s[22:23], 0, v[134:135]
	s_add_i32 m0, s62, 0x2000
	s_nop 0
	global_load_lds_dwordx4 v[214:215], off
	v_lshl_add_u64 v[214:215], s[42:43], 0, v[0:1]
	s_mov_b32 m0, s50
	s_nop 0
	global_load_lds_dwordx4 v[214:215], off
	s_mov_b32 m0, s51
	s_nop 0
	global_load_lds_dwordx4 v[216:217], off
	s_waitcnt vmcnt(8)
	s_waitcnt lgkmcnt(0)
	s_barrier
	s_setprio 1
	s_waitcnt lgkmcnt(0)
	v_mfma_f32_16x16x32_bf16 v[36:39], v[148:151], v[180:183], 0
	v_mfma_f32_16x16x32_bf16 v[28:31], v[156:159], v[180:183], 0
	v_mfma_f32_16x16x32_bf16 v[24:27], v[148:151], v[188:191], 0
	v_mfma_f32_16x16x32_bf16 v[20:23], v[156:159], v[188:191], 0
	v_mfma_f32_16x16x32_bf16 v[16:19], v[148:151], v[196:199], 0
	v_mfma_f32_16x16x32_bf16 v[12:15], v[156:159], v[196:199], 0
	v_mfma_f32_16x16x32_bf16 v[8:11], v[148:151], v[204:207], 0
	v_mfma_f32_16x16x32_bf16 v[4:7], v[156:159], v[204:207], 0
	v_mfma_f32_16x16x32_bf16 v[36:39], v[152:155], v[184:187], v[36:39]
	v_mfma_f32_16x16x32_bf16 v[28:31], v[160:163], v[184:187], v[28:31]
	v_mfma_f32_16x16x32_bf16 v[24:27], v[152:155], v[192:195], v[24:27]
	v_mfma_f32_16x16x32_bf16 v[20:23], v[160:163], v[192:195], v[20:23]
	v_mfma_f32_16x16x32_bf16 v[16:19], v[152:155], v[200:203], v[16:19]
	v_mfma_f32_16x16x32_bf16 v[12:15], v[160:163], v[200:203], v[12:15]
	v_mfma_f32_16x16x32_bf16 v[8:11], v[152:155], v[208:211], v[8:11]
	v_mfma_f32_16x16x32_bf16 v[4:7], v[160:163], v[208:211], v[4:7]
	s_setprio 0
	s_setprio 1
	v_mfma_f32_16x16x32_bf16 v[92:95], v[164:167], v[180:183], 0
	v_mfma_f32_16x16x32_bf16 v[84:87], v[172:175], v[180:183], 0
	v_mfma_f32_16x16x32_bf16 v[68:71], v[164:167], v[188:191], 0
	v_mfma_f32_16x16x32_bf16 v[60:63], v[172:175], v[188:191], 0
	v_mfma_f32_16x16x32_bf16 v[48:51], v[164:167], v[196:199], 0
	v_mfma_f32_16x16x32_bf16 v[44:47], v[172:175], v[196:199], 0
	v_mfma_f32_16x16x32_bf16 v[40:43], v[164:167], v[204:207], 0
	v_mfma_f32_16x16x32_bf16 v[32:35], v[172:175], v[204:207], 0
	v_mfma_f32_16x16x32_bf16 v[92:95], v[168:171], v[184:187], v[92:95]
	v_mfma_f32_16x16x32_bf16 v[84:87], v[176:179], v[184:187], v[84:87]
	v_mfma_f32_16x16x32_bf16 v[68:71], v[168:171], v[192:195], v[68:71]
	v_mfma_f32_16x16x32_bf16 v[60:63], v[176:179], v[192:195], v[60:63]
	v_mfma_f32_16x16x32_bf16 v[48:51], v[168:171], v[200:203], v[48:51]
	v_mfma_f32_16x16x32_bf16 v[44:47], v[176:179], v[200:203], v[44:47]
	v_mfma_f32_16x16x32_bf16 v[40:43], v[168:171], v[208:211], v[40:43]
	v_mfma_f32_16x16x32_bf16 v[32:35], v[176:179], v[208:211], v[32:35]
	s_setprio 0
	s_barrier
	s_add_i32 s62, 0, 0x18000
	s_add_i32 s63, 0, 0x1c000
	v_add_u32_e32 v160, s62, v145
	v_add_u32_e32 v176, s63, v145
	ds_read_b128 v[148:151], v160
	ds_read_b128 v[152:155], v160 offset:1024
	ds_read_b128 v[156:159], v160 offset:2048
	ds_read_b128 v[160:163], v160 offset:3072
	ds_read_b128 v[164:167], v176
	ds_read_b128 v[168:171], v176 offset:1024
	ds_read_b128 v[172:175], v176 offset:2048
	ds_read_b128 v[176:179], v176 offset:3072
	s_add_u32 s22, s42, 0x40000
	s_addc_u32 s23, s43, 0
	s_mov_b32 m0, s52
	v_lshl_add_u64 v[218:219], s[22:23], 0, v[0:1]
	ds_read_b128 v[180:183], v147 offset:32768
	ds_read_b128 v[184:187], v147 offset:33792
	ds_read_b128 v[188:191], v147 offset:34816
	ds_read_b128 v[192:195], v147 offset:35840
	ds_read_b128 v[196:199], v147 offset:36864
	ds_read_b128 v[200:203], v147 offset:37888
	ds_read_b128 v[204:207], v147 offset:38912
	ds_read_b128 v[208:211], v147 offset:39936
	global_load_lds_dwordx4 v[218:219], off
	v_lshl_add_u64 v[218:219], s[22:23], 0, v[132:133]
	s_mov_b32 m0, s53
	s_nop 0
	global_load_lds_dwordx4 v[218:219], off
	s_waitcnt vmcnt(8)
	s_waitcnt lgkmcnt(0)
	s_barrier
	s_setprio 1
	s_waitcnt lgkmcnt(0)
	v_mfma_f32_16x16x32_bf16 v[96:99], v[148:151], v[180:183], v[96:99]
	v_mfma_f32_16x16x32_bf16 v[88:91], v[156:159], v[180:183], v[88:91]
	v_mfma_f32_16x16x32_bf16 v[80:83], v[148:151], v[188:191], v[80:83]
	v_mfma_f32_16x16x32_bf16 v[76:79], v[156:159], v[188:191], v[76:79]
	v_mfma_f32_16x16x32_bf16 v[72:75], v[148:151], v[196:199], v[72:75]
	v_mfma_f32_16x16x32_bf16 v[64:67], v[156:159], v[196:199], v[64:67]
	v_mfma_f32_16x16x32_bf16 v[56:59], v[148:151], v[204:207], v[56:59]
	v_mfma_f32_16x16x32_bf16 v[52:55], v[156:159], v[204:207], v[52:55]
	v_mfma_f32_16x16x32_bf16 v[96:99], v[152:155], v[184:187], v[96:99]
	v_mfma_f32_16x16x32_bf16 v[88:91], v[160:163], v[184:187], v[88:91]
	v_mfma_f32_16x16x32_bf16 v[80:83], v[152:155], v[192:195], v[80:83]
	v_mfma_f32_16x16x32_bf16 v[76:79], v[160:163], v[192:195], v[76:79]
	v_mfma_f32_16x16x32_bf16 v[72:75], v[152:155], v[200:203], v[72:75]
	v_mfma_f32_16x16x32_bf16 v[64:67], v[160:163], v[200:203], v[64:67]
	v_mfma_f32_16x16x32_bf16 v[56:59], v[152:155], v[208:211], v[56:59]
	v_mfma_f32_16x16x32_bf16 v[52:55], v[160:163], v[208:211], v[52:55]
	s_setprio 0
	s_setprio 1
	v_mfma_f32_16x16x32_bf16 v[128:131], v[164:167], v[180:183], v[128:131]
	v_mfma_f32_16x16x32_bf16 v[124:127], v[172:175], v[180:183], v[124:127]
	v_mfma_f32_16x16x32_bf16 v[120:123], v[164:167], v[188:191], v[120:123]
	v_mfma_f32_16x16x32_bf16 v[116:119], v[172:175], v[188:191], v[116:119]
	v_mfma_f32_16x16x32_bf16 v[112:115], v[164:167], v[196:199], v[112:115]
	v_mfma_f32_16x16x32_bf16 v[108:111], v[172:175], v[196:199], v[108:111]
	v_mfma_f32_16x16x32_bf16 v[104:107], v[164:167], v[204:207], v[104:107]
	v_mfma_f32_16x16x32_bf16 v[100:103], v[172:175], v[204:207], v[100:103]
	v_mfma_f32_16x16x32_bf16 v[128:131], v[168:171], v[184:187], v[128:131]
	v_mfma_f32_16x16x32_bf16 v[124:127], v[176:179], v[184:187], v[124:127]
	v_mfma_f32_16x16x32_bf16 v[120:123], v[168:171], v[192:195], v[120:123]
	v_mfma_f32_16x16x32_bf16 v[116:119], v[176:179], v[192:195], v[116:119]
	v_mfma_f32_16x16x32_bf16 v[112:115], v[168:171], v[200:203], v[112:115]
	v_mfma_f32_16x16x32_bf16 v[108:111], v[176:179], v[200:203], v[108:111]
	v_mfma_f32_16x16x32_bf16 v[104:107], v[168:171], v[208:211], v[104:107]
	v_mfma_f32_16x16x32_bf16 v[100:103], v[176:179], v[208:211], v[100:103]
	s_setprio 0
	s_barrier
	s_add_i32 s22, s62, s47
	v_lshl_add_u64 v[142:143], v[142:143], 0, s[28:29]
	s_mov_b32 m0, s22
	ds_read_b128 v[180:183], v147 offset:49152
	ds_read_b128 v[184:187], v147 offset:50176
	ds_read_b128 v[188:191], v147 offset:51200
	ds_read_b128 v[192:195], v147 offset:52224
	ds_read_b128 v[196:199], v147 offset:53248
	ds_read_b128 v[200:203], v147 offset:54272
	ds_read_b128 v[204:207], v147 offset:55296
	ds_read_b128 v[208:211], v147 offset:56320
	global_load_lds_dwordx4 v[142:143], off
	s_add_i32 m0, s22, 0x2000
	s_add_u32 s22, s40, 0x40080
	v_lshl_add_u64 v[142:143], v[212:213], 0, s[28:29]
	s_addc_u32 s23, s41, 0
	s_add_i32 s40, s63, s47
	global_load_lds_dwordx4 v[142:143], off
	v_lshl_add_u64 v[142:143], s[22:23], 0, v[2:3]
	s_mov_b32 m0, s40
	s_nop 0
	global_load_lds_dwordx4 v[142:143], off
	v_lshl_add_u64 v[142:143], s[22:23], 0, v[134:135]
	s_add_i32 m0, s40, 0x2000
	s_nop 0
	global_load_lds_dwordx4 v[142:143], off
	v_lshl_add_u64 v[142:143], v[214:215], 0, s[28:29]
	s_mov_b32 m0, s54
	s_nop 0
	global_load_lds_dwordx4 v[142:143], off
	v_lshl_add_u64 v[142:143], v[216:217], 0, s[28:29]
	s_mov_b32 m0, s55
	s_nop 0
	global_load_lds_dwordx4 v[142:143], off
	s_waitcnt vmcnt(8)
	s_waitcnt lgkmcnt(0)
	s_barrier
	s_setprio 1
	s_waitcnt lgkmcnt(0)
	v_mfma_f32_16x16x32_bf16 v[36:39], v[148:151], v[180:183], v[36:39]
	v_mfma_f32_16x16x32_bf16 v[28:31], v[156:159], v[180:183], v[28:31]
	v_mfma_f32_16x16x32_bf16 v[24:27], v[148:151], v[188:191], v[24:27]
	v_mfma_f32_16x16x32_bf16 v[20:23], v[156:159], v[188:191], v[20:23]
	v_mfma_f32_16x16x32_bf16 v[16:19], v[148:151], v[196:199], v[16:19]
	v_mfma_f32_16x16x32_bf16 v[12:15], v[156:159], v[196:199], v[12:15]
	v_mfma_f32_16x16x32_bf16 v[8:11], v[148:151], v[204:207], v[8:11]
	v_mfma_f32_16x16x32_bf16 v[4:7], v[156:159], v[204:207], v[4:7]
	v_mfma_f32_16x16x32_bf16 v[36:39], v[152:155], v[184:187], v[36:39]
	v_mfma_f32_16x16x32_bf16 v[28:31], v[160:163], v[184:187], v[28:31]
	v_mfma_f32_16x16x32_bf16 v[24:27], v[152:155], v[192:195], v[24:27]
	v_mfma_f32_16x16x32_bf16 v[20:23], v[160:163], v[192:195], v[20:23]
	v_mfma_f32_16x16x32_bf16 v[16:19], v[152:155], v[200:203], v[16:19]
	v_mfma_f32_16x16x32_bf16 v[12:15], v[160:163], v[200:203], v[12:15]
	v_mfma_f32_16x16x32_bf16 v[8:11], v[152:155], v[208:211], v[8:11]
	v_mfma_f32_16x16x32_bf16 v[4:7], v[160:163], v[208:211], v[4:7]
	s_setprio 0
	s_setprio 1
	v_mfma_f32_16x16x32_bf16 v[92:95], v[164:167], v[180:183], v[92:95]
	v_mfma_f32_16x16x32_bf16 v[84:87], v[172:175], v[180:183], v[84:87]
	v_mfma_f32_16x16x32_bf16 v[68:71], v[164:167], v[188:191], v[68:71]
	v_mfma_f32_16x16x32_bf16 v[60:63], v[172:175], v[188:191], v[60:63]
	v_mfma_f32_16x16x32_bf16 v[48:51], v[164:167], v[196:199], v[48:51]
	v_mfma_f32_16x16x32_bf16 v[44:47], v[172:175], v[196:199], v[44:47]
	v_mfma_f32_16x16x32_bf16 v[40:43], v[164:167], v[204:207], v[40:43]
	v_mfma_f32_16x16x32_bf16 v[32:35], v[172:175], v[204:207], v[32:35]
	v_mfma_f32_16x16x32_bf16 v[92:95], v[168:171], v[184:187], v[92:95]
	v_mfma_f32_16x16x32_bf16 v[84:87], v[176:179], v[184:187], v[84:87]
	v_mfma_f32_16x16x32_bf16 v[68:71], v[168:171], v[192:195], v[68:71]
	v_mfma_f32_16x16x32_bf16 v[60:63], v[176:179], v[192:195], v[60:63]
	v_mfma_f32_16x16x32_bf16 v[48:51], v[168:171], v[200:203], v[48:51]
	v_mfma_f32_16x16x32_bf16 v[44:47], v[176:179], v[200:203], v[44:47]
	v_mfma_f32_16x16x32_bf16 v[40:43], v[168:171], v[208:211], v[40:43]
	v_mfma_f32_16x16x32_bf16 v[32:35], v[176:179], v[208:211], v[32:35]
	s_setprio 0
	s_barrier
	s_add_i32 s61, s61, 2
	s_add_u32 s59, s59, 0x100
	s_addc_u32 s60, s60, 0
	s_cmp_gt_u32 s61, 13
	s_mov_b64 s[22:23], s[26:27]
	s_cbranch_scc1 .Lmy_gx4

.Lmy_gx4:
	s_and_b64 vcc, exec, s[8:9]
	s_cbranch_vccnz .LBB0_1334
	v_lshl_add_u32 v142, s12, 8, v144
	s_cmp_eq_u32 s57, 16
	s_mov_b64 s[12:13], -1
	s_cbranch_scc0 .LBB0_1335

.LBB0_1890:
	s_ashr_i32 s15, s14, 31
	s_lshl_b64 s[16:17], s[14:15], 19
	s_add_u32 s13, s36, s16
	s_addc_u32 s15, s37, s17
	s_and_b64 s[16:17], s[38:39], exec
	s_cselect_b32 s17, s15, s21
	s_cselect_b32 s16, s13, s20
	s_ashr_i32 s13, s12, 31
	s_lshl_b64 s[18:19], s[12:13], 19
	s_add_u32 s13, s42, s18
	s_addc_u32 s15, s43, s19
	s_and_b64 s[18:19], s[38:39], exec
	s_cselect_b32 s19, s15, s23
	s_cselect_b32 s18, s13, s22
	s_add_u32 s13, s22, 0x100
	v_mov_b32_e32 v218, 0x3ecc95a3
	s_addc_u32 s15, s23, 0
	s_mov_b32 s56, -2
	s_add_u32 s22, s20, 0x100
	s_addc_u32 s23, s21, 0
	s_add_i32 s57, 0, 0x10000
	s_cmp_eq_u32 s56, 12
	s_cselect_b32 s41, s17, s23
	s_cselect_b32 s40, s16, s22
	s_cselect_b32 s27, s19, s15
	s_cselect_b32 s26, s18, s13
	s_add_i32 s58, 0, 0x14000
	v_add_u32_e32 v128, s57, v179
	v_add_u32_e32 v160, s58, v179
	ds_read_b128 v[116:119], v128
	ds_read_b128 v[120:123], v128 offset:1024
	ds_read_b128 v[124:127], v128 offset:2048
	ds_read_b128 v[128:131], v128 offset:3072
	ds_read_b128 v[148:151], v160
	ds_read_b128 v[152:155], v160 offset:1024
	ds_read_b128 v[156:159], v160 offset:2048
	ds_read_b128 v[160:163], v160 offset:3072
	v_lshl_add_u64 v[176:177], s[20:21], 0, v[170:171]
	s_add_i32 m0, s47, 0xc000
	ds_read_b128 v[172:175], v181
	ds_read_b128 v[182:185], v181 offset:1024
	ds_read_b128 v[186:189], v181 offset:2048
	ds_read_b128 v[190:193], v181 offset:3072
	ds_read_b128 v[194:197], v181 offset:4096
	ds_read_b128 v[198:201], v181 offset:5120
	ds_read_b128 v[202:205], v181 offset:6144
	ds_read_b128 v[206:209], v181 offset:7168
	global_load_lds_dwordx4 v[176:177], off
	v_lshl_add_u64 v[176:177], s[20:21], 0, v[168:169]
	s_add_i32 m0, s47, 0xe000
	s_nop 0
	global_load_lds_dwordx4 v[176:177], off
	s_waitcnt vmcnt(8)
	s_waitcnt lgkmcnt(0)
	s_barrier
	s_setprio 1
	s_waitcnt lgkmcnt(0)
	v_mfma_f32_16x16x32_bf16 v[144:147], v[116:119], v[172:175], 0
	v_mfma_f32_16x16x32_bf16 v[140:143], v[124:127], v[172:175], 0
	v_mfma_f32_16x16x32_bf16 v[112:115], v[116:119], v[186:189], 0
	v_mfma_f32_16x16x32_bf16 v[108:111], v[124:127], v[186:189], 0
	v_mfma_f32_16x16x32_bf16 v[100:103], v[116:119], v[194:197], 0
	v_mfma_f32_16x16x32_bf16 v[92:95], v[124:127], v[194:197], 0
	v_mfma_f32_16x16x32_bf16 v[84:87], v[116:119], v[202:205], 0
	v_mfma_f32_16x16x32_bf16 v[76:79], v[124:127], v[202:205], 0
	v_mfma_f32_16x16x32_bf16 v[144:147], v[120:123], v[182:185], v[144:147]
	v_mfma_f32_16x16x32_bf16 v[140:143], v[128:131], v[182:185], v[140:143]
	v_mfma_f32_16x16x32_bf16 v[112:115], v[120:123], v[190:193], v[112:115]
	v_mfma_f32_16x16x32_bf16 v[108:111], v[128:131], v[190:193], v[108:111]
	v_mfma_f32_16x16x32_bf16 v[100:103], v[120:123], v[198:201], v[100:103]
	v_mfma_f32_16x16x32_bf16 v[92:95], v[128:131], v[198:201], v[92:95]
	v_mfma_f32_16x16x32_bf16 v[84:87], v[120:123], v[206:209], v[84:87]
	v_mfma_f32_16x16x32_bf16 v[76:79], v[128:131], v[206:209], v[76:79]
	s_setprio 0
	s_setprio 1
	v_mfma_f32_16x16x32_bf16 v[136:139], v[148:151], v[172:175], 0
	v_mfma_f32_16x16x32_bf16 v[132:135], v[156:159], v[172:175], 0
	v_mfma_f32_16x16x32_bf16 v[104:107], v[148:151], v[186:189], 0
	v_mfma_f32_16x16x32_bf16 v[96:99], v[156:159], v[186:189], 0
	v_mfma_f32_16x16x32_bf16 v[88:91], v[148:151], v[194:197], 0
	v_mfma_f32_16x16x32_bf16 v[80:83], v[156:159], v[194:197], 0
	v_mfma_f32_16x16x32_bf16 v[72:75], v[148:151], v[202:205], 0
	v_mfma_f32_16x16x32_bf16 v[68:71], v[156:159], v[202:205], 0
	v_mfma_f32_16x16x32_bf16 v[136:139], v[152:155], v[182:185], v[136:139]
	v_mfma_f32_16x16x32_bf16 v[132:135], v[160:163], v[182:185], v[132:135]
	v_mfma_f32_16x16x32_bf16 v[104:107], v[152:155], v[190:193], v[104:107]
	v_mfma_f32_16x16x32_bf16 v[96:99], v[160:163], v[190:193], v[96:99]
	v_mfma_f32_16x16x32_bf16 v[88:91], v[152:155], v[198:201], v[88:91]
	v_mfma_f32_16x16x32_bf16 v[80:83], v[160:163], v[198:201], v[80:83]
	v_mfma_f32_16x16x32_bf16 v[72:75], v[152:155], v[206:209], v[72:75]
	v_mfma_f32_16x16x32_bf16 v[68:71], v[160:163], v[206:209], v[68:71]
	s_setprio 0
	s_barrier
	s_add_i32 s20, s57, s46
	v_lshl_add_u64 v[176:177], s[26:27], 0, v[2:3]
	s_mov_b32 m0, s20
	ds_read_b128 v[172:175], v181 offset:16384
	ds_read_b128 v[182:185], v181 offset:17408
	ds_read_b128 v[186:189], v181 offset:18432
	ds_read_b128 v[190:193], v181 offset:19456
	ds_read_b128 v[194:197], v181 offset:20480
	ds_read_b128 v[198:201], v181 offset:21504
	ds_read_b128 v[202:205], v181 offset:22528
	ds_read_b128 v[206:209], v181 offset:23552
	global_load_lds_dwordx4 v[176:177], off
	s_add_i32 m0, s20, 0x2000
	s_add_u32 s20, s26, 0x40000
	v_lshl_add_u64 v[210:211], s[26:27], 0, v[166:167]
	s_addc_u32 s21, s27, 0
	s_add_i32 s57, s58, s46
	global_load_lds_dwordx4 v[210:211], off
	v_lshl_add_u64 v[212:213], s[20:21], 0, v[2:3]
	s_mov_b32 m0, s57
	v_lshl_add_u64 v[214:215], s[40:41], 0, v[164:165]
	global_load_lds_dwordx4 v[212:213], off
	v_lshl_add_u64 v[212:213], s[20:21], 0, v[166:167]
	s_add_i32 m0, s57, 0x2000
	s_nop 0
	global_load_lds_dwordx4 v[212:213], off
	v_lshl_add_u64 v[212:213], s[40:41], 0, v[0:1]
	s_mov_b32 m0, s47
	s_nop 0
	global_load_lds_dwordx4 v[212:213], off
	s_mov_b32 m0, s48
	s_nop 0
	global_load_lds_dwordx4 v[214:215], off
	s_waitcnt vmcnt(8)
	s_waitcnt lgkmcnt(0)
	s_barrier
	s_setprio 1
	s_waitcnt lgkmcnt(0)
	v_mfma_f32_16x16x32_bf16 v[64:67], v[116:119], v[172:175], 0
	v_mfma_f32_16x16x32_bf16 v[60:63], v[124:127], v[172:175], 0
	v_mfma_f32_16x16x32_bf16 v[48:51], v[116:119], v[186:189], 0
	v_mfma_f32_16x16x32_bf16 v[44:47], v[124:127], v[186:189], 0
	v_mfma_f32_16x16x32_bf16 v[36:39], v[116:119], v[194:197], 0
	v_mfma_f32_16x16x32_bf16 v[28:31], v[124:127], v[194:197], 0
	v_mfma_f32_16x16x32_bf16 v[20:23], v[116:119], v[202:205], 0
	v_mfma_f32_16x16x32_bf16 v[12:15], v[124:127], v[202:205], 0
	v_mfma_f32_16x16x32_bf16 v[64:67], v[120:123], v[182:185], v[64:67]
	v_mfma_f32_16x16x32_bf16 v[60:63], v[128:131], v[182:185], v[60:63]
	v_mfma_f32_16x16x32_bf16 v[48:51], v[120:123], v[190:193], v[48:51]
	v_mfma_f32_16x16x32_bf16 v[44:47], v[128:131], v[190:193], v[44:47]
	v_mfma_f32_16x16x32_bf16 v[36:39], v[120:123], v[198:201], v[36:39]
	v_mfma_f32_16x16x32_bf16 v[28:31], v[128:131], v[198:201], v[28:31]
	v_mfma_f32_16x16x32_bf16 v[20:23], v[120:123], v[206:209], v[20:23]
	v_mfma_f32_16x16x32_bf16 v[12:15], v[128:131], v[206:209], v[12:15]
	s_setprio 0
	s_setprio 1
	v_mfma_f32_16x16x32_bf16 v[56:59], v[148:151], v[172:175], 0
	v_mfma_f32_16x16x32_bf16 v[52:55], v[156:159], v[172:175], 0
	v_mfma_f32_16x16x32_bf16 v[40:43], v[148:151], v[186:189], 0
	v_mfma_f32_16x16x32_bf16 v[32:35], v[156:159], v[186:189], 0
	v_mfma_f32_16x16x32_bf16 v[24:27], v[148:151], v[194:197], 0
	v_mfma_f32_16x16x32_bf16 v[16:19], v[156:159], v[194:197], 0
	v_mfma_f32_16x16x32_bf16 v[8:11], v[148:151], v[202:205], 0
	v_mfma_f32_16x16x32_bf16 v[4:7], v[156:159], v[202:205], 0
	v_mfma_f32_16x16x32_bf16 v[56:59], v[152:155], v[182:185], v[56:59]
	v_mfma_f32_16x16x32_bf16 v[52:55], v[160:163], v[182:185], v[52:55]
	v_mfma_f32_16x16x32_bf16 v[40:43], v[152:155], v[190:193], v[40:43]
	v_mfma_f32_16x16x32_bf16 v[32:35], v[160:163], v[190:193], v[32:35]
	v_mfma_f32_16x16x32_bf16 v[24:27], v[152:155], v[198:201], v[24:27]
	v_mfma_f32_16x16x32_bf16 v[16:19], v[160:163], v[198:201], v[16:19]
	v_mfma_f32_16x16x32_bf16 v[8:11], v[152:155], v[206:209], v[8:11]
	v_mfma_f32_16x16x32_bf16 v[4:7], v[160:163], v[206:209], v[4:7]
	s_setprio 0
	s_barrier
	s_add_i32 s57, 0, 0x18000
	s_add_i32 s58, 0, 0x1c000
	v_add_u32_e32 v128, s57, v179
	v_add_u32_e32 v160, s58, v179
	ds_read_b128 v[116:119], v128
	ds_read_b128 v[120:123], v128 offset:1024
	ds_read_b128 v[124:127], v128 offset:2048
	ds_read_b128 v[128:131], v128 offset:3072
	ds_read_b128 v[148:151], v160
	ds_read_b128 v[152:155], v160 offset:1024
	ds_read_b128 v[156:159], v160 offset:2048
	ds_read_b128 v[160:163], v160 offset:3072
	s_add_u32 s20, s40, 0x40000
	s_addc_u32 s21, s41, 0
	s_mov_b32 m0, s49
	v_lshl_add_u64 v[216:217], s[20:21], 0, v[0:1]
	ds_read_b128 v[172:175], v181 offset:32768
	ds_read_b128 v[182:185], v181 offset:33792
	ds_read_b128 v[186:189], v181 offset:34816
	ds_read_b128 v[190:193], v181 offset:35840
	ds_read_b128 v[194:197], v181 offset:36864
	ds_read_b128 v[198:201], v181 offset:37888
	ds_read_b128 v[202:205], v181 offset:38912
	ds_read_b128 v[206:209], v181 offset:39936
	global_load_lds_dwordx4 v[216:217], off
	v_lshl_add_u64 v[216:217], s[20:21], 0, v[164:165]
	s_mov_b32 m0, s50
	s_nop 0
	global_load_lds_dwordx4 v[216:217], off
	s_waitcnt vmcnt(8)
	s_waitcnt lgkmcnt(0)
	s_barrier
	s_setprio 1
	s_waitcnt lgkmcnt(0)
	v_mfma_f32_16x16x32_bf16 v[144:147], v[116:119], v[172:175], v[144:147]
	v_mfma_f32_16x16x32_bf16 v[140:143], v[124:127], v[172:175], v[140:143]
	v_mfma_f32_16x16x32_bf16 v[112:115], v[116:119], v[186:189], v[112:115]
	v_mfma_f32_16x16x32_bf16 v[108:111], v[124:127], v[186:189], v[108:111]
	v_mfma_f32_16x16x32_bf16 v[100:103], v[116:119], v[194:197], v[100:103]
	v_mfma_f32_16x16x32_bf16 v[92:95], v[124:127], v[194:197], v[92:95]
	v_mfma_f32_16x16x32_bf16 v[84:87], v[116:119], v[202:205], v[84:87]
	v_mfma_f32_16x16x32_bf16 v[76:79], v[124:127], v[202:205], v[76:79]
	v_mfma_f32_16x16x32_bf16 v[144:147], v[120:123], v[182:185], v[144:147]
	v_mfma_f32_16x16x32_bf16 v[140:143], v[128:131], v[182:185], v[140:143]
	v_mfma_f32_16x16x32_bf16 v[112:115], v[120:123], v[190:193], v[112:115]
	v_mfma_f32_16x16x32_bf16 v[108:111], v[128:131], v[190:193], v[108:111]
	v_mfma_f32_16x16x32_bf16 v[100:103], v[120:123], v[198:201], v[100:103]
	v_mfma_f32_16x16x32_bf16 v[92:95], v[128:131], v[198:201], v[92:95]
	v_mfma_f32_16x16x32_bf16 v[84:87], v[120:123], v[206:209], v[84:87]
	v_mfma_f32_16x16x32_bf16 v[76:79], v[128:131], v[206:209], v[76:79]
	s_setprio 0
	s_setprio 1
	v_mfma_f32_16x16x32_bf16 v[136:139], v[148:151], v[172:175], v[136:139]
	v_mfma_f32_16x16x32_bf16 v[132:135], v[156:159], v[172:175], v[132:135]
	v_mfma_f32_16x16x32_bf16 v[104:107], v[148:151], v[186:189], v[104:107]
	v_mfma_f32_16x16x32_bf16 v[96:99], v[156:159], v[186:189], v[96:99]
	v_mfma_f32_16x16x32_bf16 v[88:91], v[148:151], v[194:197], v[88:91]
	v_mfma_f32_16x16x32_bf16 v[80:83], v[156:159], v[194:197], v[80:83]
	v_mfma_f32_16x16x32_bf16 v[72:75], v[148:151], v[202:205], v[72:75]
	v_mfma_f32_16x16x32_bf16 v[68:71], v[156:159], v[202:205], v[68:71]
	v_mfma_f32_16x16x32_bf16 v[136:139], v[152:155], v[182:185], v[136:139]
	v_mfma_f32_16x16x32_bf16 v[132:135], v[160:163], v[182:185], v[132:135]
	v_mfma_f32_16x16x32_bf16 v[104:107], v[152:155], v[190:193], v[104:107]
	v_mfma_f32_16x16x32_bf16 v[96:99], v[160:163], v[190:193], v[96:99]
	v_mfma_f32_16x16x32_bf16 v[88:91], v[152:155], v[198:201], v[88:91]
	v_mfma_f32_16x16x32_bf16 v[80:83], v[160:163], v[198:201], v[80:83]
	v_mfma_f32_16x16x32_bf16 v[72:75], v[152:155], v[206:209], v[72:75]
	v_mfma_f32_16x16x32_bf16 v[68:71], v[160:163], v[206:209], v[68:71]
	s_setprio 0
	s_barrier
	s_add_i32 s20, s57, s46
	v_lshl_add_u64 v[176:177], v[176:177], 0, s[28:29]
	s_mov_b32 m0, s20
	ds_read_b128 v[172:175], v181 offset:49152
	ds_read_b128 v[182:185], v181 offset:50176
	ds_read_b128 v[186:189], v181 offset:51200
	ds_read_b128 v[190:193], v181 offset:52224
	ds_read_b128 v[194:197], v181 offset:53248
	ds_read_b128 v[198:201], v181 offset:54272
	ds_read_b128 v[202:205], v181 offset:55296
	ds_read_b128 v[206:209], v181 offset:56320
	global_load_lds_dwordx4 v[176:177], off
	s_add_i32 m0, s20, 0x2000
	s_add_u32 s20, s26, 0x40080
	v_lshl_add_u64 v[176:177], v[210:211], 0, s[28:29]
	s_addc_u32 s21, s27, 0
	s_add_i32 s26, s58, s46
	global_load_lds_dwordx4 v[176:177], off
	v_lshl_add_u64 v[176:177], s[20:21], 0, v[2:3]
	s_mov_b32 m0, s26
	s_nop 0
	global_load_lds_dwordx4 v[176:177], off
	v_lshl_add_u64 v[176:177], s[20:21], 0, v[166:167]
	s_add_i32 m0, s26, 0x2000
	s_nop 0
	global_load_lds_dwordx4 v[176:177], off
	v_lshl_add_u64 v[176:177], v[212:213], 0, s[28:29]
	s_mov_b32 m0, s53
	s_nop 0
	global_load_lds_dwordx4 v[176:177], off
	v_lshl_add_u64 v[176:177], v[214:215], 0, s[28:29]
	s_mov_b32 m0, s54
	s_nop 0
	global_load_lds_dwordx4 v[176:177], off
	s_waitcnt vmcnt(8)
	s_waitcnt lgkmcnt(0)
	s_barrier
	s_setprio 1
	s_waitcnt lgkmcnt(0)
	v_mfma_f32_16x16x32_bf16 v[64:67], v[116:119], v[172:175], v[64:67]
	v_mfma_f32_16x16x32_bf16 v[60:63], v[124:127], v[172:175], v[60:63]
	v_mfma_f32_16x16x32_bf16 v[48:51], v[116:119], v[186:189], v[48:51]
	v_mfma_f32_16x16x32_bf16 v[44:47], v[124:127], v[186:189], v[44:47]
	v_mfma_f32_16x16x32_bf16 v[36:39], v[116:119], v[194:197], v[36:39]
	v_mfma_f32_16x16x32_bf16 v[28:31], v[124:127], v[194:197], v[28:31]
	v_mfma_f32_16x16x32_bf16 v[20:23], v[116:119], v[202:205], v[20:23]
	v_mfma_f32_16x16x32_bf16 v[12:15], v[124:127], v[202:205], v[12:15]
	v_mfma_f32_16x16x32_bf16 v[64:67], v[120:123], v[182:185], v[64:67]
	v_mfma_f32_16x16x32_bf16 v[60:63], v[128:131], v[182:185], v[60:63]
	v_mfma_f32_16x16x32_bf16 v[48:51], v[120:123], v[190:193], v[48:51]
	v_mfma_f32_16x16x32_bf16 v[44:47], v[128:131], v[190:193], v[44:47]
	v_mfma_f32_16x16x32_bf16 v[36:39], v[120:123], v[198:201], v[36:39]
	v_mfma_f32_16x16x32_bf16 v[28:31], v[128:131], v[198:201], v[28:31]
	v_mfma_f32_16x16x32_bf16 v[20:23], v[120:123], v[206:209], v[20:23]
	v_mfma_f32_16x16x32_bf16 v[12:15], v[128:131], v[206:209], v[12:15]
	s_setprio 0
	s_setprio 1
	v_mfma_f32_16x16x32_bf16 v[56:59], v[148:151], v[172:175], v[56:59]
	v_mfma_f32_16x16x32_bf16 v[52:55], v[156:159], v[172:175], v[52:55]
	v_mfma_f32_16x16x32_bf16 v[40:43], v[148:151], v[186:189], v[40:43]
	v_mfma_f32_16x16x32_bf16 v[32:35], v[156:159], v[186:189], v[32:35]
	v_mfma_f32_16x16x32_bf16 v[24:27], v[148:151], v[194:197], v[24:27]
	v_mfma_f32_16x16x32_bf16 v[16:19], v[156:159], v[194:197], v[16:19]
	v_mfma_f32_16x16x32_bf16 v[8:11], v[148:151], v[202:205], v[8:11]
	v_mfma_f32_16x16x32_bf16 v[4:7], v[156:159], v[202:205], v[4:7]
	v_mfma_f32_16x16x32_bf16 v[56:59], v[152:155], v[182:185], v[56:59]
	v_mfma_f32_16x16x32_bf16 v[52:55], v[160:163], v[182:185], v[52:55]
	v_mfma_f32_16x16x32_bf16 v[40:43], v[152:155], v[190:193], v[40:43]
	v_mfma_f32_16x16x32_bf16 v[32:35], v[160:163], v[190:193], v[32:35]
	v_mfma_f32_16x16x32_bf16 v[24:27], v[152:155], v[198:201], v[24:27]
	v_mfma_f32_16x16x32_bf16 v[16:19], v[160:163], v[198:201], v[16:19]
	v_mfma_f32_16x16x32_bf16 v[8:11], v[152:155], v[206:209], v[8:11]
	v_mfma_f32_16x16x32_bf16 v[4:7], v[160:163], v[206:209], v[4:7]
	s_setprio 0
	s_barrier
	s_add_i32 s56, s56, 2
	s_add_u32 s13, s13, 0x100
	s_addc_u32 s15, s15, 0
	s_cmp_gt_u32 s56, 13
	s_mov_b64 s[20:21], s[22:23]
	s_cbranch_scc1 .Lmy_gx5

.LBB0_2282:
	s_ashr_i32 s15, s14, 31
	s_lshl_b64 s[16:17], s[14:15], 19
	s_add_u32 s20, s58, s16
	s_addc_u32 s21, s59, s17
	s_and_b64 s[16:17], s[38:39], exec
	s_cselect_b32 s11, s21, s41
	s_cselect_b32 s15, s20, s40
	s_ashr_i32 s19, s18, 31
	s_lshl_b64 s[16:17], s[18:19], 19
	s_add_u32 s22, s60, s16
	s_addc_u32 s23, s61, s17
	s_and_b64 s[16:17], s[38:39], exec
	s_cselect_b32 s16, s23, s43
	s_cselect_b32 s17, s22, s42
	s_add_u32 s19, s42, 0x100
	s_addc_u32 s73, s43, 0
	s_mov_b32 s76, -2
	s_add_u32 s42, s40, 0x100
	s_addc_u32 s43, s41, 0
	s_add_i32 s77, 0, 0x10000
	s_cmp_eq_u32 s76, 12
	s_cselect_b32 s47, s11, s43
	s_cselect_b32 s46, s15, s42
	s_cselect_b32 s45, s16, s73
	s_cselect_b32 s44, s17, s19
	s_add_i32 s78, 0, 0x14000
	v_add_u32_e32 v156, s77, v141
	v_add_u32_e32 v172, s78, v141
	ds_read_b128 v[144:147], v156
	ds_read_b128 v[148:151], v156 offset:1024
	ds_read_b128 v[152:155], v156 offset:2048
	ds_read_b128 v[156:159], v156 offset:3072
	ds_read_b128 v[160:163], v172
	ds_read_b128 v[164:167], v172 offset:1024
	ds_read_b128 v[168:171], v172 offset:2048
	ds_read_b128 v[172:175], v172 offset:3072
	v_lshl_add_u64 v[208:209], s[40:41], 0, v[138:139]
	s_add_i32 m0, s27, 0xc000
	ds_read_b128 v[176:179], v143
	ds_read_b128 v[180:183], v143 offset:1024
	ds_read_b128 v[184:187], v143 offset:2048
	ds_read_b128 v[188:191], v143 offset:3072
	ds_read_b128 v[192:195], v143 offset:4096
	ds_read_b128 v[196:199], v143 offset:5120
	ds_read_b128 v[200:203], v143 offset:6144
	ds_read_b128 v[204:207], v143 offset:7168
	global_load_lds_dwordx4 v[208:209], off
	v_lshl_add_u64 v[208:209], s[40:41], 0, v[136:137]
	s_add_i32 m0, s27, 0xe000
	s_nop 0
	global_load_lds_dwordx4 v[208:209], off
	s_waitcnt vmcnt(8)
	s_waitcnt lgkmcnt(0)
	s_barrier
	s_setprio 1
	s_waitcnt lgkmcnt(0)
	v_mfma_f32_16x16x32_bf16 v[128:131], v[144:147], v[176:179], 0
	v_mfma_f32_16x16x32_bf16 v[120:123], v[152:155], v[176:179], 0
	v_mfma_f32_16x16x32_bf16 v[112:115], v[144:147], v[184:187], 0
	v_mfma_f32_16x16x32_bf16 v[104:107], v[152:155], v[184:187], 0
	v_mfma_f32_16x16x32_bf16 v[96:99], v[144:147], v[192:195], 0
	v_mfma_f32_16x16x32_bf16 v[88:91], v[152:155], v[192:195], 0
	v_mfma_f32_16x16x32_bf16 v[80:83], v[144:147], v[200:203], 0
	v_mfma_f32_16x16x32_bf16 v[72:75], v[152:155], v[200:203], 0
	v_mfma_f32_16x16x32_bf16 v[128:131], v[148:151], v[180:183], v[128:131]
	v_mfma_f32_16x16x32_bf16 v[120:123], v[156:159], v[180:183], v[120:123]
	v_mfma_f32_16x16x32_bf16 v[112:115], v[148:151], v[188:191], v[112:115]
	v_mfma_f32_16x16x32_bf16 v[104:107], v[156:159], v[188:191], v[104:107]
	v_mfma_f32_16x16x32_bf16 v[96:99], v[148:151], v[196:199], v[96:99]
	v_mfma_f32_16x16x32_bf16 v[88:91], v[156:159], v[196:199], v[88:91]
	v_mfma_f32_16x16x32_bf16 v[80:83], v[148:151], v[204:207], v[80:83]
	v_mfma_f32_16x16x32_bf16 v[72:75], v[156:159], v[204:207], v[72:75]
	s_setprio 0
	s_setprio 1
	v_mfma_f32_16x16x32_bf16 v[124:127], v[160:163], v[176:179], 0
	v_mfma_f32_16x16x32_bf16 v[116:119], v[168:171], v[176:179], 0
	v_mfma_f32_16x16x32_bf16 v[108:111], v[160:163], v[184:187], 0
	v_mfma_f32_16x16x32_bf16 v[100:103], v[168:171], v[184:187], 0
	v_mfma_f32_16x16x32_bf16 v[92:95], v[160:163], v[192:195], 0
	v_mfma_f32_16x16x32_bf16 v[84:87], v[168:171], v[192:195], 0
	v_mfma_f32_16x16x32_bf16 v[76:79], v[160:163], v[200:203], 0
	v_mfma_f32_16x16x32_bf16 v[68:71], v[168:171], v[200:203], 0
	v_mfma_f32_16x16x32_bf16 v[124:127], v[164:167], v[180:183], v[124:127]
	v_mfma_f32_16x16x32_bf16 v[116:119], v[172:175], v[180:183], v[116:119]
	v_mfma_f32_16x16x32_bf16 v[108:111], v[164:167], v[188:191], v[108:111]
	v_mfma_f32_16x16x32_bf16 v[100:103], v[172:175], v[188:191], v[100:103]
	v_mfma_f32_16x16x32_bf16 v[92:95], v[164:167], v[196:199], v[92:95]
	v_mfma_f32_16x16x32_bf16 v[84:87], v[172:175], v[196:199], v[84:87]
	v_mfma_f32_16x16x32_bf16 v[76:79], v[164:167], v[204:207], v[76:79]
	v_mfma_f32_16x16x32_bf16 v[68:71], v[172:175], v[204:207], v[68:71]
	s_setprio 0
	s_barrier
	s_add_i32 s40, s77, s62
	v_lshl_add_u64 v[208:209], s[44:45], 0, v[2:3]
	s_mov_b32 m0, s40
	ds_read_b128 v[176:179], v143 offset:16384
	ds_read_b128 v[180:183], v143 offset:17408
	ds_read_b128 v[184:187], v143 offset:18432
	ds_read_b128 v[188:191], v143 offset:19456
	ds_read_b128 v[192:195], v143 offset:20480
	ds_read_b128 v[196:199], v143 offset:21504
	ds_read_b128 v[200:203], v143 offset:22528
	ds_read_b128 v[204:207], v143 offset:23552
	global_load_lds_dwordx4 v[208:209], off
	s_add_i32 m0, s40, 0x2000
	s_add_u32 s40, s44, 0x40000
	v_lshl_add_u64 v[210:211], s[44:45], 0, v[134:135]
	s_addc_u32 s41, s45, 0
	s_add_i32 s77, s78, s62
	global_load_lds_dwordx4 v[210:211], off
	v_lshl_add_u64 v[212:213], s[40:41], 0, v[2:3]
	s_mov_b32 m0, s77
	v_lshl_add_u64 v[214:215], s[46:47], 0, v[132:133]
	global_load_lds_dwordx4 v[212:213], off
	v_lshl_add_u64 v[212:213], s[40:41], 0, v[134:135]
	s_add_i32 m0, s77, 0x2000
	s_nop 0
	global_load_lds_dwordx4 v[212:213], off
	v_lshl_add_u64 v[212:213], s[46:47], 0, v[0:1]
	s_mov_b32 m0, s27
	s_nop 0
	global_load_lds_dwordx4 v[212:213], off
	s_mov_b32 m0, s63
	s_nop 0
	global_load_lds_dwordx4 v[214:215], off
	s_waitcnt vmcnt(8)
	s_waitcnt lgkmcnt(0)
	s_barrier
	s_setprio 1
	s_waitcnt lgkmcnt(0)
	v_mfma_f32_16x16x32_bf16 v[64:67], v[144:147], v[176:179], 0
	v_mfma_f32_16x16x32_bf16 v[56:59], v[152:155], v[176:179], 0
	v_mfma_f32_16x16x32_bf16 v[48:51], v[144:147], v[184:187], 0
	v_mfma_f32_16x16x32_bf16 v[40:43], v[152:155], v[184:187], 0
	v_mfma_f32_16x16x32_bf16 v[32:35], v[144:147], v[192:195], 0
	v_mfma_f32_16x16x32_bf16 v[24:27], v[152:155], v[192:195], 0
	v_mfma_f32_16x16x32_bf16 v[16:19], v[144:147], v[200:203], 0
	v_mfma_f32_16x16x32_bf16 v[8:11], v[152:155], v[200:203], 0
	v_mfma_f32_16x16x32_bf16 v[64:67], v[148:151], v[180:183], v[64:67]
	v_mfma_f32_16x16x32_bf16 v[56:59], v[156:159], v[180:183], v[56:59]
	v_mfma_f32_16x16x32_bf16 v[48:51], v[148:151], v[188:191], v[48:51]
	v_mfma_f32_16x16x32_bf16 v[40:43], v[156:159], v[188:191], v[40:43]
	v_mfma_f32_16x16x32_bf16 v[32:35], v[148:151], v[196:199], v[32:35]
	v_mfma_f32_16x16x32_bf16 v[24:27], v[156:159], v[196:199], v[24:27]
	v_mfma_f32_16x16x32_bf16 v[16:19], v[148:151], v[204:207], v[16:19]
	v_mfma_f32_16x16x32_bf16 v[8:11], v[156:159], v[204:207], v[8:11]
	s_setprio 0
	s_setprio 1
	v_mfma_f32_16x16x32_bf16 v[60:63], v[160:163], v[176:179], 0
	v_mfma_f32_16x16x32_bf16 v[52:55], v[168:171], v[176:179], 0
	v_mfma_f32_16x16x32_bf16 v[44:47], v[160:163], v[184:187], 0
	v_mfma_f32_16x16x32_bf16 v[36:39], v[168:171], v[184:187], 0
	v_mfma_f32_16x16x32_bf16 v[28:31], v[160:163], v[192:195], 0
	v_mfma_f32_16x16x32_bf16 v[20:23], v[168:171], v[192:195], 0
	v_mfma_f32_16x16x32_bf16 v[12:15], v[160:163], v[200:203], 0
	v_mfma_f32_16x16x32_bf16 v[4:7], v[168:171], v[200:203], 0
	v_mfma_f32_16x16x32_bf16 v[60:63], v[164:167], v[180:183], v[60:63]
	v_mfma_f32_16x16x32_bf16 v[52:55], v[172:175], v[180:183], v[52:55]
	v_mfma_f32_16x16x32_bf16 v[44:47], v[164:167], v[188:191], v[44:47]
	v_mfma_f32_16x16x32_bf16 v[36:39], v[172:175], v[188:191], v[36:39]
	v_mfma_f32_16x16x32_bf16 v[28:31], v[164:167], v[196:199], v[28:31]
	v_mfma_f32_16x16x32_bf16 v[20:23], v[172:175], v[196:199], v[20:23]
	v_mfma_f32_16x16x32_bf16 v[12:15], v[164:167], v[204:207], v[12:15]
	v_mfma_f32_16x16x32_bf16 v[4:7], v[172:175], v[204:207], v[4:7]
	s_setprio 0
	s_barrier
	s_add_i32 s77, 0, 0x18000
	s_add_i32 s78, 0, 0x1c000
	v_add_u32_e32 v156, s77, v141
	v_add_u32_e32 v172, s78, v141
	ds_read_b128 v[144:147], v156
	ds_read_b128 v[148:151], v156 offset:1024
	ds_read_b128 v[152:155], v156 offset:2048
	ds_read_b128 v[156:159], v156 offset:3072
	ds_read_b128 v[160:163], v172
	ds_read_b128 v[164:167], v172 offset:1024
	ds_read_b128 v[168:171], v172 offset:2048
	ds_read_b128 v[172:175], v172 offset:3072
	s_add_u32 s40, s46, 0x40000
	s_addc_u32 s41, s47, 0
	s_mov_b32 m0, s68
	v_lshl_add_u64 v[216:217], s[40:41], 0, v[0:1]
	ds_read_b128 v[176:179], v143 offset:32768
	ds_read_b128 v[180:183], v143 offset:33792
	ds_read_b128 v[184:187], v143 offset:34816
	ds_read_b128 v[188:191], v143 offset:35840
	ds_read_b128 v[192:195], v143 offset:36864
	ds_read_b128 v[196:199], v143 offset:37888
	ds_read_b128 v[200:203], v143 offset:38912
	ds_read_b128 v[204:207], v143 offset:39936
	global_load_lds_dwordx4 v[216:217], off
	v_lshl_add_u64 v[216:217], s[40:41], 0, v[132:133]
	s_mov_b32 m0, s69
	s_nop 0
	global_load_lds_dwordx4 v[216:217], off
	s_waitcnt vmcnt(8)
	s_waitcnt lgkmcnt(0)
	s_barrier
	s_setprio 1
	s_waitcnt lgkmcnt(0)
	v_mfma_f32_16x16x32_bf16 v[128:131], v[144:147], v[176:179], v[128:131]
	v_mfma_f32_16x16x32_bf16 v[120:123], v[152:155], v[176:179], v[120:123]
	v_mfma_f32_16x16x32_bf16 v[112:115], v[144:147], v[184:187], v[112:115]
	v_mfma_f32_16x16x32_bf16 v[104:107], v[152:155], v[184:187], v[104:107]
	v_mfma_f32_16x16x32_bf16 v[96:99], v[144:147], v[192:195], v[96:99]
	v_mfma_f32_16x16x32_bf16 v[88:91], v[152:155], v[192:195], v[88:91]
	v_mfma_f32_16x16x32_bf16 v[80:83], v[144:147], v[200:203], v[80:83]
	v_mfma_f32_16x16x32_bf16 v[72:75], v[152:155], v[200:203], v[72:75]
	v_mfma_f32_16x16x32_bf16 v[128:131], v[148:151], v[180:183], v[128:131]
	v_mfma_f32_16x16x32_bf16 v[120:123], v[156:159], v[180:183], v[120:123]
	v_mfma_f32_16x16x32_bf16 v[112:115], v[148:151], v[188:191], v[112:115]
	v_mfma_f32_16x16x32_bf16 v[104:107], v[156:159], v[188:191], v[104:107]
	v_mfma_f32_16x16x32_bf16 v[96:99], v[148:151], v[196:199], v[96:99]
	v_mfma_f32_16x16x32_bf16 v[88:91], v[156:159], v[196:199], v[88:91]
	v_mfma_f32_16x16x32_bf16 v[80:83], v[148:151], v[204:207], v[80:83]
	v_mfma_f32_16x16x32_bf16 v[72:75], v[156:159], v[204:207], v[72:75]
	s_setprio 0
	s_setprio 1
	v_mfma_f32_16x16x32_bf16 v[124:127], v[160:163], v[176:179], v[124:127]
	v_mfma_f32_16x16x32_bf16 v[116:119], v[168:171], v[176:179], v[116:119]
	v_mfma_f32_16x16x32_bf16 v[108:111], v[160:163], v[184:187], v[108:111]
	v_mfma_f32_16x16x32_bf16 v[100:103], v[168:171], v[184:187], v[100:103]
	v_mfma_f32_16x16x32_bf16 v[92:95], v[160:163], v[192:195], v[92:95]
	v_mfma_f32_16x16x32_bf16 v[84:87], v[168:171], v[192:195], v[84:87]
	v_mfma_f32_16x16x32_bf16 v[76:79], v[160:163], v[200:203], v[76:79]
	v_mfma_f32_16x16x32_bf16 v[68:71], v[168:171], v[200:203], v[68:71]
	v_mfma_f32_16x16x32_bf16 v[124:127], v[164:167], v[180:183], v[124:127]
	v_mfma_f32_16x16x32_bf16 v[116:119], v[172:175], v[180:183], v[116:119]
	v_mfma_f32_16x16x32_bf16 v[108:111], v[164:167], v[188:191], v[108:111]
	v_mfma_f32_16x16x32_bf16 v[100:103], v[172:175], v[188:191], v[100:103]
	v_mfma_f32_16x16x32_bf16 v[92:95], v[164:167], v[196:199], v[92:95]
	v_mfma_f32_16x16x32_bf16 v[84:87], v[172:175], v[196:199], v[84:87]
	v_mfma_f32_16x16x32_bf16 v[76:79], v[164:167], v[204:207], v[76:79]
	v_mfma_f32_16x16x32_bf16 v[68:71], v[172:175], v[204:207], v[68:71]
	s_setprio 0
	s_barrier
	s_add_i32 s40, s77, s62
	v_lshl_add_u64 v[208:209], v[208:209], 0, s[28:29]
	s_mov_b32 m0, s40
	ds_read_b128 v[176:179], v143 offset:49152
	ds_read_b128 v[180:183], v143 offset:50176
	ds_read_b128 v[184:187], v143 offset:51200
	ds_read_b128 v[188:191], v143 offset:52224
	ds_read_b128 v[192:195], v143 offset:53248
	ds_read_b128 v[196:199], v143 offset:54272
	ds_read_b128 v[200:203], v143 offset:55296
	ds_read_b128 v[204:207], v143 offset:56320
	global_load_lds_dwordx4 v[208:209], off
	s_add_i32 m0, s40, 0x2000
	s_add_u32 s40, s44, 0x40080
	v_lshl_add_u64 v[208:209], v[210:211], 0, s[28:29]
	s_addc_u32 s41, s45, 0
	s_add_i32 s44, s78, s62
	global_load_lds_dwordx4 v[208:209], off
	v_lshl_add_u64 v[208:209], s[40:41], 0, v[2:3]
	s_mov_b32 m0, s44
	s_nop 0
	global_load_lds_dwordx4 v[208:209], off
	v_lshl_add_u64 v[208:209], s[40:41], 0, v[134:135]
	s_add_i32 m0, s44, 0x2000
	s_nop 0
	global_load_lds_dwordx4 v[208:209], off
	v_lshl_add_u64 v[208:209], v[212:213], 0, s[28:29]
	s_mov_b32 m0, s70
	s_nop 0
	global_load_lds_dwordx4 v[208:209], off
	v_lshl_add_u64 v[208:209], v[214:215], 0, s[28:29]
	s_mov_b32 m0, s71
	s_nop 0
	global_load_lds_dwordx4 v[208:209], off
	s_waitcnt vmcnt(8)
	s_waitcnt lgkmcnt(0)
	s_barrier
	s_setprio 1
	s_waitcnt lgkmcnt(0)
	v_mfma_f32_16x16x32_bf16 v[64:67], v[144:147], v[176:179], v[64:67]
	v_mfma_f32_16x16x32_bf16 v[56:59], v[152:155], v[176:179], v[56:59]
	v_mfma_f32_16x16x32_bf16 v[48:51], v[144:147], v[184:187], v[48:51]
	v_mfma_f32_16x16x32_bf16 v[40:43], v[152:155], v[184:187], v[40:43]
	v_mfma_f32_16x16x32_bf16 v[32:35], v[144:147], v[192:195], v[32:35]
	v_mfma_f32_16x16x32_bf16 v[24:27], v[152:155], v[192:195], v[24:27]
	v_mfma_f32_16x16x32_bf16 v[16:19], v[144:147], v[200:203], v[16:19]
	v_mfma_f32_16x16x32_bf16 v[8:11], v[152:155], v[200:203], v[8:11]
	v_mfma_f32_16x16x32_bf16 v[64:67], v[148:151], v[180:183], v[64:67]
	v_mfma_f32_16x16x32_bf16 v[56:59], v[156:159], v[180:183], v[56:59]
	v_mfma_f32_16x16x32_bf16 v[48:51], v[148:151], v[188:191], v[48:51]
	v_mfma_f32_16x16x32_bf16 v[40:43], v[156:159], v[188:191], v[40:43]
	v_mfma_f32_16x16x32_bf16 v[32:35], v[148:151], v[196:199], v[32:35]
	v_mfma_f32_16x16x32_bf16 v[24:27], v[156:159], v[196:199], v[24:27]
	v_mfma_f32_16x16x32_bf16 v[16:19], v[148:151], v[204:207], v[16:19]
	v_mfma_f32_16x16x32_bf16 v[8:11], v[156:159], v[204:207], v[8:11]
	s_setprio 0
	s_setprio 1
	v_mfma_f32_16x16x32_bf16 v[60:63], v[160:163], v[176:179], v[60:63]
	v_mfma_f32_16x16x32_bf16 v[52:55], v[168:171], v[176:179], v[52:55]
	v_mfma_f32_16x16x32_bf16 v[44:47], v[160:163], v[184:187], v[44:47]
	v_mfma_f32_16x16x32_bf16 v[36:39], v[168:171], v[184:187], v[36:39]
	v_mfma_f32_16x16x32_bf16 v[28:31], v[160:163], v[192:195], v[28:31]
	v_mfma_f32_16x16x32_bf16 v[20:23], v[168:171], v[192:195], v[20:23]
	v_mfma_f32_16x16x32_bf16 v[12:15], v[160:163], v[200:203], v[12:15]
	v_mfma_f32_16x16x32_bf16 v[4:7], v[168:171], v[200:203], v[4:7]
	v_mfma_f32_16x16x32_bf16 v[60:63], v[164:167], v[180:183], v[60:63]
	v_mfma_f32_16x16x32_bf16 v[52:55], v[172:175], v[180:183], v[52:55]
	v_mfma_f32_16x16x32_bf16 v[44:47], v[164:167], v[188:191], v[44:47]
	v_mfma_f32_16x16x32_bf16 v[36:39], v[172:175], v[188:191], v[36:39]
	v_mfma_f32_16x16x32_bf16 v[28:31], v[164:167], v[196:199], v[28:31]
	v_mfma_f32_16x16x32_bf16 v[20:23], v[172:175], v[196:199], v[20:23]
	v_mfma_f32_16x16x32_bf16 v[12:15], v[164:167], v[204:207], v[12:15]
	v_mfma_f32_16x16x32_bf16 v[4:7], v[172:175], v[204:207], v[4:7]
	s_setprio 0
	s_barrier
	s_add_i32 s76, s76, 2
	s_add_u32 s19, s19, 0x100
	s_addc_u32 s73, s73, 0
	s_cmp_gt_u32 s76, 13
	s_mov_b64 s[40:41], s[42:43]
	s_cbranch_scc1 .Lmy_gx6

.LBB0_2350:
	s_add_u32 s58, s18, 0x100
	s_addc_u32 s59, s19, 0
	s_mov_b32 s60, -2
	s_add_u32 s18, s14, 0x100
	s_addc_u32 s19, s15, 0
	s_add_i32 s61, 0, 0x10000
	s_cmp_eq_u32 s60, 52
	s_cselect_b32 s23, s11, s19
	s_cselect_b32 s22, s10, s18
	s_cselect_b32 s21, s13, s59
	s_cselect_b32 s20, s12, s58
	s_add_i32 s62, 0, 0x14000
	v_add_u32_e32 v156, s61, v141
	v_add_u32_e32 v172, s62, v141
	ds_read_b128 v[144:147], v156
	ds_read_b128 v[148:151], v156 offset:1024
	ds_read_b128 v[152:155], v156 offset:2048
	ds_read_b128 v[156:159], v156 offset:3072
	ds_read_b128 v[160:163], v172
	ds_read_b128 v[164:167], v172 offset:1024
	ds_read_b128 v[168:171], v172 offset:2048
	ds_read_b128 v[172:175], v172 offset:3072
	v_lshl_add_u64 v[208:209], s[14:15], 0, v[138:139]
	s_add_i32 m0, s47, 0xc000
	ds_read_b128 v[176:179], v143
	ds_read_b128 v[180:183], v143 offset:1024
	ds_read_b128 v[184:187], v143 offset:2048
	ds_read_b128 v[188:191], v143 offset:3072
	ds_read_b128 v[192:195], v143 offset:4096
	ds_read_b128 v[196:199], v143 offset:5120
	ds_read_b128 v[200:203], v143 offset:6144
	ds_read_b128 v[204:207], v143 offset:7168
	global_load_lds_dwordx4 v[208:209], off
	v_lshl_add_u64 v[208:209], s[14:15], 0, v[136:137]
	s_add_i32 m0, s47, 0xe000
	s_nop 0
	global_load_lds_dwordx4 v[208:209], off
	s_waitcnt vmcnt(8)
	s_waitcnt lgkmcnt(0)
	s_barrier
	s_setprio 1
	s_waitcnt lgkmcnt(0)
	v_mfma_f32_16x16x32_bf16 v[128:131], v[144:147], v[176:179], 0
	v_mfma_f32_16x16x32_bf16 v[124:127], v[152:155], v[176:179], 0
	v_mfma_f32_16x16x32_bf16 v[120:123], v[144:147], v[184:187], 0
	v_mfma_f32_16x16x32_bf16 v[116:119], v[152:155], v[184:187], 0
	v_mfma_f32_16x16x32_bf16 v[104:107], v[144:147], v[192:195], 0
	v_mfma_f32_16x16x32_bf16 v[100:103], v[152:155], v[192:195], 0
	v_mfma_f32_16x16x32_bf16 v[88:91], v[144:147], v[200:203], 0
	v_mfma_f32_16x16x32_bf16 v[84:87], v[152:155], v[200:203], 0
	v_mfma_f32_16x16x32_bf16 v[128:131], v[148:151], v[180:183], v[128:131]
	v_mfma_f32_16x16x32_bf16 v[124:127], v[156:159], v[180:183], v[124:127]
	v_mfma_f32_16x16x32_bf16 v[120:123], v[148:151], v[188:191], v[120:123]
	v_mfma_f32_16x16x32_bf16 v[116:119], v[156:159], v[188:191], v[116:119]
	v_mfma_f32_16x16x32_bf16 v[104:107], v[148:151], v[196:199], v[104:107]
	v_mfma_f32_16x16x32_bf16 v[100:103], v[156:159], v[196:199], v[100:103]
	v_mfma_f32_16x16x32_bf16 v[88:91], v[148:151], v[204:207], v[88:91]
	v_mfma_f32_16x16x32_bf16 v[84:87], v[156:159], v[204:207], v[84:87]
	s_setprio 0
	s_setprio 1
	v_mfma_f32_16x16x32_bf16 v[112:115], v[160:163], v[176:179], 0
	v_mfma_f32_16x16x32_bf16 v[108:111], v[168:171], v[176:179], 0
	v_mfma_f32_16x16x32_bf16 v[96:99], v[160:163], v[184:187], 0
	v_mfma_f32_16x16x32_bf16 v[92:95], v[168:171], v[184:187], 0
	v_mfma_f32_16x16x32_bf16 v[80:83], v[160:163], v[192:195], 0
	v_mfma_f32_16x16x32_bf16 v[76:79], v[168:171], v[192:195], 0
	v_mfma_f32_16x16x32_bf16 v[72:75], v[160:163], v[200:203], 0
	v_mfma_f32_16x16x32_bf16 v[68:71], v[168:171], v[200:203], 0
	v_mfma_f32_16x16x32_bf16 v[112:115], v[164:167], v[180:183], v[112:115]
	v_mfma_f32_16x16x32_bf16 v[108:111], v[172:175], v[180:183], v[108:111]
	v_mfma_f32_16x16x32_bf16 v[96:99], v[164:167], v[188:191], v[96:99]
	v_mfma_f32_16x16x32_bf16 v[92:95], v[172:175], v[188:191], v[92:95]
	v_mfma_f32_16x16x32_bf16 v[80:83], v[164:167], v[196:199], v[80:83]
	v_mfma_f32_16x16x32_bf16 v[76:79], v[172:175], v[196:199], v[76:79]
	v_mfma_f32_16x16x32_bf16 v[72:75], v[164:167], v[204:207], v[72:75]
	v_mfma_f32_16x16x32_bf16 v[68:71], v[172:175], v[204:207], v[68:71]
	s_setprio 0
	s_barrier
	s_add_i32 s14, s61, s45
	v_lshl_add_u64 v[208:209], s[20:21], 0, v[2:3]
	s_mov_b32 m0, s14
	ds_read_b128 v[176:179], v143 offset:16384
	ds_read_b128 v[180:183], v143 offset:17408
	ds_read_b128 v[184:187], v143 offset:18432
	ds_read_b128 v[188:191], v143 offset:19456
	ds_read_b128 v[192:195], v143 offset:20480
	ds_read_b128 v[196:199], v143 offset:21504
	ds_read_b128 v[200:203], v143 offset:22528
	ds_read_b128 v[204:207], v143 offset:23552
	global_load_lds_dwordx4 v[208:209], off
	s_add_i32 m0, s14, 0x2000
	s_add_u32 s14, s20, 0xe0000
	v_lshl_add_u64 v[210:211], s[20:21], 0, v[0:1]
	s_addc_u32 s15, s21, 0
	s_add_i32 s61, s62, s45
	global_load_lds_dwordx4 v[210:211], off
	v_lshl_add_u64 v[212:213], s[14:15], 0, v[2:3]
	s_mov_b32 m0, s61
	v_lshl_add_u64 v[214:215], s[22:23], 0, v[132:133]
	global_load_lds_dwordx4 v[212:213], off
	v_lshl_add_u64 v[212:213], s[14:15], 0, v[0:1]
	s_add_i32 m0, s61, 0x2000
	s_nop 0
	global_load_lds_dwordx4 v[212:213], off
	v_lshl_add_u64 v[212:213], s[22:23], 0, v[134:135]
	s_mov_b32 m0, s47
	s_nop 0
	global_load_lds_dwordx4 v[212:213], off
	s_mov_b32 m0, s48
	s_nop 0
	global_load_lds_dwordx4 v[214:215], off
	s_waitcnt vmcnt(8)
	s_waitcnt lgkmcnt(0)
	s_barrier
	s_setprio 1
	s_waitcnt lgkmcnt(0)
	v_mfma_f32_16x16x32_bf16 v[64:67], v[144:147], v[176:179], 0
	v_mfma_f32_16x16x32_bf16 v[60:63], v[152:155], v[176:179], 0
	v_mfma_f32_16x16x32_bf16 v[56:59], v[144:147], v[184:187], 0
	v_mfma_f32_16x16x32_bf16 v[52:55], v[152:155], v[184:187], 0
	v_mfma_f32_16x16x32_bf16 v[40:43], v[144:147], v[192:195], 0
	v_mfma_f32_16x16x32_bf16 v[36:39], v[152:155], v[192:195], 0
	v_mfma_f32_16x16x32_bf16 v[24:27], v[144:147], v[200:203], 0
	v_mfma_f32_16x16x32_bf16 v[20:23], v[152:155], v[200:203], 0
	v_mfma_f32_16x16x32_bf16 v[64:67], v[148:151], v[180:183], v[64:67]
	v_mfma_f32_16x16x32_bf16 v[60:63], v[156:159], v[180:183], v[60:63]
	v_mfma_f32_16x16x32_bf16 v[56:59], v[148:151], v[188:191], v[56:59]
	v_mfma_f32_16x16x32_bf16 v[52:55], v[156:159], v[188:191], v[52:55]
	v_mfma_f32_16x16x32_bf16 v[40:43], v[148:151], v[196:199], v[40:43]
	v_mfma_f32_16x16x32_bf16 v[36:39], v[156:159], v[196:199], v[36:39]
	v_mfma_f32_16x16x32_bf16 v[24:27], v[148:151], v[204:207], v[24:27]
	v_mfma_f32_16x16x32_bf16 v[20:23], v[156:159], v[204:207], v[20:23]
	s_setprio 0
	s_setprio 1
	v_mfma_f32_16x16x32_bf16 v[48:51], v[160:163], v[176:179], 0
	v_mfma_f32_16x16x32_bf16 v[44:47], v[168:171], v[176:179], 0
	v_mfma_f32_16x16x32_bf16 v[32:35], v[160:163], v[184:187], 0
	v_mfma_f32_16x16x32_bf16 v[28:31], v[168:171], v[184:187], 0
	v_mfma_f32_16x16x32_bf16 v[16:19], v[160:163], v[192:195], 0
	v_mfma_f32_16x16x32_bf16 v[12:15], v[168:171], v[192:195], 0
	v_mfma_f32_16x16x32_bf16 v[8:11], v[160:163], v[200:203], 0
	v_mfma_f32_16x16x32_bf16 v[4:7], v[168:171], v[200:203], 0
	v_mfma_f32_16x16x32_bf16 v[48:51], v[164:167], v[180:183], v[48:51]
	v_mfma_f32_16x16x32_bf16 v[44:47], v[172:175], v[180:183], v[44:47]
	v_mfma_f32_16x16x32_bf16 v[32:35], v[164:167], v[188:191], v[32:35]
	v_mfma_f32_16x16x32_bf16 v[28:31], v[172:175], v[188:191], v[28:31]
	v_mfma_f32_16x16x32_bf16 v[16:19], v[164:167], v[196:199], v[16:19]
	v_mfma_f32_16x16x32_bf16 v[12:15], v[172:175], v[196:199], v[12:15]
	v_mfma_f32_16x16x32_bf16 v[8:11], v[164:167], v[204:207], v[8:11]
	v_mfma_f32_16x16x32_bf16 v[4:7], v[172:175], v[204:207], v[4:7]
	s_setprio 0
	s_barrier
	s_add_i32 s61, 0, 0x18000
	s_add_i32 s62, 0, 0x1c000
	v_add_u32_e32 v156, s61, v141
	v_add_u32_e32 v172, s62, v141
	ds_read_b128 v[144:147], v156
	ds_read_b128 v[148:151], v156 offset:1024
	ds_read_b128 v[152:155], v156 offset:2048
	ds_read_b128 v[156:159], v156 offset:3072
	ds_read_b128 v[160:163], v172
	ds_read_b128 v[164:167], v172 offset:1024
	ds_read_b128 v[168:171], v172 offset:2048
	ds_read_b128 v[172:175], v172 offset:3072
	s_add_u32 s14, s22, 0xe0000
	s_addc_u32 s15, s23, 0
	s_mov_b32 m0, s49
	v_lshl_add_u64 v[216:217], s[14:15], 0, v[134:135]
	ds_read_b128 v[176:179], v143 offset:32768
	ds_read_b128 v[180:183], v143 offset:33792
	ds_read_b128 v[184:187], v143 offset:34816
	ds_read_b128 v[188:191], v143 offset:35840
	ds_read_b128 v[192:195], v143 offset:36864
	ds_read_b128 v[196:199], v143 offset:37888
	ds_read_b128 v[200:203], v143 offset:38912
	ds_read_b128 v[204:207], v143 offset:39936
	global_load_lds_dwordx4 v[216:217], off
	v_lshl_add_u64 v[216:217], s[14:15], 0, v[132:133]
	s_mov_b32 m0, s50
	s_nop 0
	global_load_lds_dwordx4 v[216:217], off
	s_waitcnt vmcnt(8)
	s_waitcnt lgkmcnt(0)
	s_barrier
	s_setprio 1
	s_waitcnt lgkmcnt(0)
	v_mfma_f32_16x16x32_bf16 v[128:131], v[144:147], v[176:179], v[128:131]
	v_mfma_f32_16x16x32_bf16 v[124:127], v[152:155], v[176:179], v[124:127]
	v_mfma_f32_16x16x32_bf16 v[120:123], v[144:147], v[184:187], v[120:123]
	v_mfma_f32_16x16x32_bf16 v[116:119], v[152:155], v[184:187], v[116:119]
	v_mfma_f32_16x16x32_bf16 v[104:107], v[144:147], v[192:195], v[104:107]
	v_mfma_f32_16x16x32_bf16 v[100:103], v[152:155], v[192:195], v[100:103]
	v_mfma_f32_16x16x32_bf16 v[88:91], v[144:147], v[200:203], v[88:91]
	v_mfma_f32_16x16x32_bf16 v[84:87], v[152:155], v[200:203], v[84:87]
	v_mfma_f32_16x16x32_bf16 v[128:131], v[148:151], v[180:183], v[128:131]
	v_mfma_f32_16x16x32_bf16 v[124:127], v[156:159], v[180:183], v[124:127]
	v_mfma_f32_16x16x32_bf16 v[120:123], v[148:151], v[188:191], v[120:123]
	v_mfma_f32_16x16x32_bf16 v[116:119], v[156:159], v[188:191], v[116:119]
	v_mfma_f32_16x16x32_bf16 v[104:107], v[148:151], v[196:199], v[104:107]
	v_mfma_f32_16x16x32_bf16 v[100:103], v[156:159], v[196:199], v[100:103]
	v_mfma_f32_16x16x32_bf16 v[88:91], v[148:151], v[204:207], v[88:91]
	v_mfma_f32_16x16x32_bf16 v[84:87], v[156:159], v[204:207], v[84:87]
	s_setprio 0
	s_setprio 1
	v_mfma_f32_16x16x32_bf16 v[112:115], v[160:163], v[176:179], v[112:115]
	v_mfma_f32_16x16x32_bf16 v[108:111], v[168:171], v[176:179], v[108:111]
	v_mfma_f32_16x16x32_bf16 v[96:99], v[160:163], v[184:187], v[96:99]
	v_mfma_f32_16x16x32_bf16 v[92:95], v[168:171], v[184:187], v[92:95]
	v_mfma_f32_16x16x32_bf16 v[80:83], v[160:163], v[192:195], v[80:83]
	v_mfma_f32_16x16x32_bf16 v[76:79], v[168:171], v[192:195], v[76:79]
	v_mfma_f32_16x16x32_bf16 v[72:75], v[160:163], v[200:203], v[72:75]
	v_mfma_f32_16x16x32_bf16 v[68:71], v[168:171], v[200:203], v[68:71]
	v_mfma_f32_16x16x32_bf16 v[112:115], v[164:167], v[180:183], v[112:115]
	v_mfma_f32_16x16x32_bf16 v[108:111], v[172:175], v[180:183], v[108:111]
	v_mfma_f32_16x16x32_bf16 v[96:99], v[164:167], v[188:191], v[96:99]
	v_mfma_f32_16x16x32_bf16 v[92:95], v[172:175], v[188:191], v[92:95]
	v_mfma_f32_16x16x32_bf16 v[80:83], v[164:167], v[196:199], v[80:83]
	v_mfma_f32_16x16x32_bf16 v[76:79], v[172:175], v[196:199], v[76:79]
	v_mfma_f32_16x16x32_bf16 v[72:75], v[164:167], v[204:207], v[72:75]
	v_mfma_f32_16x16x32_bf16 v[68:71], v[172:175], v[204:207], v[68:71]
	s_setprio 0
	s_barrier
	s_add_i32 s14, s61, s45
	v_lshl_add_u64 v[208:209], v[208:209], 0, s[28:29]
	s_mov_b32 m0, s14
	ds_read_b128 v[176:179], v143 offset:49152
	ds_read_b128 v[180:183], v143 offset:50176
	ds_read_b128 v[184:187], v143 offset:51200
	ds_read_b128 v[188:191], v143 offset:52224
	ds_read_b128 v[192:195], v143 offset:53248
	ds_read_b128 v[196:199], v143 offset:54272
	ds_read_b128 v[200:203], v143 offset:55296
	ds_read_b128 v[204:207], v143 offset:56320
	global_load_lds_dwordx4 v[208:209], off
	s_add_i32 m0, s14, 0x2000
	s_add_u32 s14, s20, 0xe0080
	v_lshl_add_u64 v[208:209], v[210:211], 0, s[28:29]
	s_addc_u32 s15, s21, 0
	s_add_i32 s20, s62, s45
	global_load_lds_dwordx4 v[208:209], off
	v_lshl_add_u64 v[208:209], s[14:15], 0, v[2:3]
	s_mov_b32 m0, s20
	s_nop 0
	global_load_lds_dwordx4 v[208:209], off
	v_lshl_add_u64 v[208:209], s[14:15], 0, v[0:1]
	s_add_i32 m0, s20, 0x2000
	s_nop 0
	global_load_lds_dwordx4 v[208:209], off
	v_lshl_add_u64 v[208:209], v[212:213], 0, s[28:29]
	s_mov_b32 m0, s51
	s_nop 0
	global_load_lds_dwordx4 v[208:209], off
	v_lshl_add_u64 v[208:209], v[214:215], 0, s[28:29]
	s_mov_b32 m0, s52
	s_nop 0
	global_load_lds_dwordx4 v[208:209], off
	s_waitcnt vmcnt(8)
	s_waitcnt lgkmcnt(0)
	s_barrier
	s_setprio 1
	s_waitcnt lgkmcnt(0)
	v_mfma_f32_16x16x32_bf16 v[64:67], v[144:147], v[176:179], v[64:67]
	v_mfma_f32_16x16x32_bf16 v[60:63], v[152:155], v[176:179], v[60:63]
	v_mfma_f32_16x16x32_bf16 v[56:59], v[144:147], v[184:187], v[56:59]
	v_mfma_f32_16x16x32_bf16 v[52:55], v[152:155], v[184:187], v[52:55]
	v_mfma_f32_16x16x32_bf16 v[40:43], v[144:147], v[192:195], v[40:43]
	v_mfma_f32_16x16x32_bf16 v[36:39], v[152:155], v[192:195], v[36:39]
	v_mfma_f32_16x16x32_bf16 v[24:27], v[144:147], v[200:203], v[24:27]
	v_mfma_f32_16x16x32_bf16 v[20:23], v[152:155], v[200:203], v[20:23]
	v_mfma_f32_16x16x32_bf16 v[64:67], v[148:151], v[180:183], v[64:67]
	v_mfma_f32_16x16x32_bf16 v[60:63], v[156:159], v[180:183], v[60:63]
	v_mfma_f32_16x16x32_bf16 v[56:59], v[148:151], v[188:191], v[56:59]
	v_mfma_f32_16x16x32_bf16 v[52:55], v[156:159], v[188:191], v[52:55]
	v_mfma_f32_16x16x32_bf16 v[40:43], v[148:151], v[196:199], v[40:43]
	v_mfma_f32_16x16x32_bf16 v[36:39], v[156:159], v[196:199], v[36:39]
	v_mfma_f32_16x16x32_bf16 v[24:27], v[148:151], v[204:207], v[24:27]
	v_mfma_f32_16x16x32_bf16 v[20:23], v[156:159], v[204:207], v[20:23]
	s_setprio 0
	s_setprio 1
	v_mfma_f32_16x16x32_bf16 v[48:51], v[160:163], v[176:179], v[48:51]
	v_mfma_f32_16x16x32_bf16 v[44:47], v[168:171], v[176:179], v[44:47]
	v_mfma_f32_16x16x32_bf16 v[32:35], v[160:163], v[184:187], v[32:35]
	v_mfma_f32_16x16x32_bf16 v[28:31], v[168:171], v[184:187], v[28:31]
	v_mfma_f32_16x16x32_bf16 v[16:19], v[160:163], v[192:195], v[16:19]
	v_mfma_f32_16x16x32_bf16 v[12:15], v[168:171], v[192:195], v[12:15]
	v_mfma_f32_16x16x32_bf16 v[8:11], v[160:163], v[200:203], v[8:11]
	v_mfma_f32_16x16x32_bf16 v[4:7], v[168:171], v[200:203], v[4:7]
	v_mfma_f32_16x16x32_bf16 v[48:51], v[164:167], v[180:183], v[48:51]
	v_mfma_f32_16x16x32_bf16 v[44:47], v[172:175], v[180:183], v[44:47]
	v_mfma_f32_16x16x32_bf16 v[32:35], v[164:167], v[188:191], v[32:35]
	v_mfma_f32_16x16x32_bf16 v[28:31], v[172:175], v[188:191], v[28:31]
	v_mfma_f32_16x16x32_bf16 v[16:19], v[164:167], v[196:199], v[16:19]
	v_mfma_f32_16x16x32_bf16 v[12:15], v[172:175], v[196:199], v[12:15]
	v_mfma_f32_16x16x32_bf16 v[8:11], v[164:167], v[204:207], v[8:11]
	v_mfma_f32_16x16x32_bf16 v[4:7], v[172:175], v[204:207], v[4:7]
	s_setprio 0
	s_barrier
	s_add_i32 s60, s60, 2
	s_add_u32 s58, s58, 0x100
	s_addc_u32 s59, s59, 0
	s_cmp_gt_u32 s60, 53
	s_mov_b64 s[14:15], s[18:19]
	s_cbranch_scc1 .Lmy_gx7

.LBB0_2373:
	s_mov_b64 s[70:71], 0x100
	v_lshl_add_u64 v[140:141], v[4:5], 0, s[70:71]
	s_mov_b32 s16, 0
	s_mov_b64 s[72:73], 0xe0000
	s_mov_b64 s[76:77], 0xe0080
	s_add_i32 s17, s16, 2
	s_add_u32 s18, s14, 0x100
	s_addc_u32 s19, s15, 0
	s_add_i32 s69, 0, 0x10000
	s_cmp_eq_u32 s62, s16
	s_cselect_b32 s21, s13, s19
	s_cselect_b32 s20, s12, s18
	v_add_u32_e32 v2, s69, v143
	s_cselect_b64 vcc, -1, 0
	s_add_i32 s16, 0, 0x14000
	ds_read_b128 v[148:151], v2
	ds_read_b128 v[152:155], v2 offset:1024
	ds_read_b128 v[156:159], v2 offset:2048
	ds_read_b128 v[160:163], v2 offset:3072
	v_add_u32_e32 v2, s16, v143
	ds_read_b128 v[164:167], v2
	ds_read_b128 v[168:171], v2 offset:1024
	ds_read_b128 v[172:175], v2 offset:2048
	ds_read_b128 v[176:179], v2 offset:3072
	v_cndmask_b32_e32 v213, v141, v139, vcc
	v_cndmask_b32_e32 v212, v140, v138, vcc
	v_lshl_add_u64 v[214:215], s[14:15], 0, v[136:137]
	s_add_i32 m0, s50, 0xc000
	ds_read_b128 v[180:183], v146
	ds_read_b128 v[184:187], v146 offset:1024
	ds_read_b128 v[188:191], v146 offset:2048
	ds_read_b128 v[192:195], v146 offset:3072
	ds_read_b128 v[196:199], v146 offset:4096
	ds_read_b128 v[200:203], v146 offset:5120
	ds_read_b128 v[204:207], v146 offset:6144
	ds_read_b128 v[208:211], v146 offset:7168
	global_load_lds_dwordx4 v[214:215], off
	v_lshl_add_u64 v[214:215], s[14:15], 0, v[134:135]
	s_add_i32 m0, s50, 0xe000
	s_nop 0
	global_load_lds_dwordx4 v[214:215], off
	s_waitcnt vmcnt(8)
	s_waitcnt lgkmcnt(0)
	s_barrier
	s_setprio 1
	s_waitcnt lgkmcnt(0)
	v_mfma_f32_16x16x32_bf16 v[128:131], v[148:151], v[180:183], 0
	v_mfma_f32_16x16x32_bf16 v[124:127], v[156:159], v[180:183], 0
	v_mfma_f32_16x16x32_bf16 v[120:123], v[148:151], v[188:191], 0
	v_mfma_f32_16x16x32_bf16 v[116:119], v[156:159], v[188:191], 0
	v_mfma_f32_16x16x32_bf16 v[108:111], v[148:151], v[196:199], 0
	v_mfma_f32_16x16x32_bf16 v[100:103], v[156:159], v[196:199], 0
	v_mfma_f32_16x16x32_bf16 v[92:95], v[148:151], v[204:207], 0
	v_mfma_f32_16x16x32_bf16 v[84:87], v[156:159], v[204:207], 0
	v_mfma_f32_16x16x32_bf16 v[128:131], v[152:155], v[184:187], v[128:131]
	v_mfma_f32_16x16x32_bf16 v[124:127], v[160:163], v[184:187], v[124:127]
	v_mfma_f32_16x16x32_bf16 v[120:123], v[152:155], v[192:195], v[120:123]
	v_mfma_f32_16x16x32_bf16 v[116:119], v[160:163], v[192:195], v[116:119]
	v_mfma_f32_16x16x32_bf16 v[108:111], v[152:155], v[200:203], v[108:111]
	v_mfma_f32_16x16x32_bf16 v[100:103], v[160:163], v[200:203], v[100:103]
	v_mfma_f32_16x16x32_bf16 v[92:95], v[152:155], v[208:211], v[92:95]
	v_mfma_f32_16x16x32_bf16 v[84:87], v[160:163], v[208:211], v[84:87]
	s_setprio 0
	s_setprio 1
	v_mfma_f32_16x16x32_bf16 v[112:115], v[164:167], v[180:183], 0
	v_mfma_f32_16x16x32_bf16 v[104:107], v[172:175], v[180:183], 0
	v_mfma_f32_16x16x32_bf16 v[96:99], v[164:167], v[188:191], 0
	v_mfma_f32_16x16x32_bf16 v[88:91], v[172:175], v[188:191], 0
	v_mfma_f32_16x16x32_bf16 v[80:83], v[164:167], v[196:199], 0
	v_mfma_f32_16x16x32_bf16 v[76:79], v[172:175], v[196:199], 0
	v_mfma_f32_16x16x32_bf16 v[72:75], v[164:167], v[204:207], 0
	v_mfma_f32_16x16x32_bf16 v[68:71], v[172:175], v[204:207], 0
	v_mfma_f32_16x16x32_bf16 v[112:115], v[168:171], v[184:187], v[112:115]
	v_mfma_f32_16x16x32_bf16 v[104:107], v[176:179], v[184:187], v[104:107]
	v_mfma_f32_16x16x32_bf16 v[96:99], v[168:171], v[192:195], v[96:99]
	v_mfma_f32_16x16x32_bf16 v[88:91], v[176:179], v[192:195], v[88:91]
	v_mfma_f32_16x16x32_bf16 v[80:83], v[168:171], v[200:203], v[80:83]
	v_mfma_f32_16x16x32_bf16 v[76:79], v[176:179], v[200:203], v[76:79]
	v_mfma_f32_16x16x32_bf16 v[72:75], v[168:171], v[208:211], v[72:75]
	v_mfma_f32_16x16x32_bf16 v[68:71], v[176:179], v[208:211], v[68:71]
	s_setprio 0
	s_barrier
	s_add_i32 s14, s69, s45
	v_lshl_add_u64 v[214:215], v[212:213], 0, v[132:133]
	s_mov_b32 m0, s14
	ds_read_b128 v[180:183], v146 offset:16384
	ds_read_b128 v[184:187], v146 offset:17408
	ds_read_b128 v[188:191], v146 offset:18432
	ds_read_b128 v[192:195], v146 offset:19456
	ds_read_b128 v[196:199], v146 offset:20480
	ds_read_b128 v[200:203], v146 offset:21504
	ds_read_b128 v[204:207], v146 offset:22528
	ds_read_b128 v[208:211], v146 offset:23552
	global_load_lds_dwordx4 v[214:215], off
	v_lshl_add_u64 v[216:217], v[212:213], 0, v[0:1]
	s_add_i32 m0, s14, 0x2000
	v_lshl_add_u64 v[218:219], v[212:213], 0, s[72:73]
	s_add_i32 s14, s16, s45
	global_load_lds_dwordx4 v[216:217], off
	v_lshl_add_u64 v[220:221], v[218:219], 0, v[132:133]
	s_mov_b32 m0, s14
	v_lshl_add_u64 v[218:219], v[218:219], 0, v[0:1]
	global_load_lds_dwordx4 v[220:221], off
	s_add_i32 m0, s14, 0x2000
	v_lshl_add_u64 v[220:221], s[20:21], 0, v[0:1]
	global_load_lds_dwordx4 v[218:219], off
	v_lshl_add_u64 v[218:219], s[20:21], 0, v[132:133]
	s_mov_b32 m0, s50
	s_nop 0
	global_load_lds_dwordx4 v[218:219], off
	s_mov_b32 m0, s51
	s_nop 0
	global_load_lds_dwordx4 v[220:221], off
	s_waitcnt vmcnt(8)
	s_waitcnt lgkmcnt(0)
	s_barrier
	s_setprio 1
	s_waitcnt lgkmcnt(0)
	v_mfma_f32_16x16x32_bf16 v[64:67], v[148:151], v[180:183], 0
	v_mfma_f32_16x16x32_bf16 v[60:63], v[156:159], v[180:183], 0
	v_mfma_f32_16x16x32_bf16 v[56:59], v[148:151], v[188:191], 0
	v_mfma_f32_16x16x32_bf16 v[52:55], v[156:159], v[188:191], 0
	v_mfma_f32_16x16x32_bf16 v[40:43], v[148:151], v[196:199], 0
	v_mfma_f32_16x16x32_bf16 v[36:39], v[156:159], v[196:199], 0
	v_mfma_f32_16x16x32_bf16 v[24:27], v[148:151], v[204:207], 0
	v_mfma_f32_16x16x32_bf16 v[20:23], v[156:159], v[204:207], 0
	v_mfma_f32_16x16x32_bf16 v[64:67], v[152:155], v[184:187], v[64:67]
	v_mfma_f32_16x16x32_bf16 v[60:63], v[160:163], v[184:187], v[60:63]
	v_mfma_f32_16x16x32_bf16 v[56:59], v[152:155], v[192:195], v[56:59]
	v_mfma_f32_16x16x32_bf16 v[52:55], v[160:163], v[192:195], v[52:55]
	v_mfma_f32_16x16x32_bf16 v[40:43], v[152:155], v[200:203], v[40:43]
	v_mfma_f32_16x16x32_bf16 v[36:39], v[160:163], v[200:203], v[36:39]
	v_mfma_f32_16x16x32_bf16 v[24:27], v[152:155], v[208:211], v[24:27]
	v_mfma_f32_16x16x32_bf16 v[20:23], v[160:163], v[208:211], v[20:23]
	s_setprio 0
	s_setprio 1
	v_mfma_f32_16x16x32_bf16 v[48:51], v[164:167], v[180:183], 0
	v_mfma_f32_16x16x32_bf16 v[44:47], v[172:175], v[180:183], 0
	v_mfma_f32_16x16x32_bf16 v[32:35], v[164:167], v[188:191], 0
	v_mfma_f32_16x16x32_bf16 v[28:31], v[172:175], v[188:191], 0
	v_mfma_f32_16x16x32_bf16 v[16:19], v[164:167], v[196:199], 0
	v_mfma_f32_16x16x32_bf16 v[12:15], v[172:175], v[196:199], 0
	v_mfma_f32_16x16x32_bf16 v[8:11], v[164:167], v[204:207], 0
	v_mfma_f32_16x16x32_bf16 v[4:7], v[172:175], v[204:207], 0
	v_mfma_f32_16x16x32_bf16 v[48:51], v[168:171], v[184:187], v[48:51]
	v_mfma_f32_16x16x32_bf16 v[44:47], v[176:179], v[184:187], v[44:47]
	v_mfma_f32_16x16x32_bf16 v[32:35], v[168:171], v[192:195], v[32:35]
	v_mfma_f32_16x16x32_bf16 v[28:31], v[176:179], v[192:195], v[28:31]
	v_mfma_f32_16x16x32_bf16 v[16:19], v[168:171], v[200:203], v[16:19]
	v_mfma_f32_16x16x32_bf16 v[12:15], v[176:179], v[200:203], v[12:15]
	v_mfma_f32_16x16x32_bf16 v[8:11], v[168:171], v[208:211], v[8:11]
	v_mfma_f32_16x16x32_bf16 v[4:7], v[176:179], v[208:211], v[4:7]
	s_setprio 0
	s_barrier
	s_add_i32 s16, 0, 0x18000
	v_add_u32_e32 v2, s16, v143
	s_add_i32 s69, 0, 0x1c000
	ds_read_b128 v[148:151], v2
	ds_read_b128 v[152:155], v2 offset:1024
	ds_read_b128 v[156:159], v2 offset:2048
	ds_read_b128 v[160:163], v2 offset:3072
	v_add_u32_e32 v2, s69, v143
	ds_read_b128 v[164:167], v2
	ds_read_b128 v[168:171], v2 offset:1024
	ds_read_b128 v[172:175], v2 offset:2048
	ds_read_b128 v[176:179], v2 offset:3072
	s_add_u32 s14, s20, 0xe0000
	s_addc_u32 s15, s21, 0
	s_mov_b32 m0, s52
	v_lshl_add_u64 v[222:223], s[14:15], 0, v[132:133]
	ds_read_b128 v[180:183], v146 offset:32768
	ds_read_b128 v[184:187], v146 offset:33792
	ds_read_b128 v[188:191], v146 offset:34816
	ds_read_b128 v[192:195], v146 offset:35840
	ds_read_b128 v[196:199], v146 offset:36864
	ds_read_b128 v[200:203], v146 offset:37888
	ds_read_b128 v[204:207], v146 offset:38912
	ds_read_b128 v[208:211], v146 offset:39936
	global_load_lds_dwordx4 v[222:223], off
	v_lshl_add_u64 v[222:223], s[14:15], 0, v[0:1]
	s_mov_b32 m0, s53
	s_nop 0
	global_load_lds_dwordx4 v[222:223], off
	s_waitcnt vmcnt(8)
	s_waitcnt lgkmcnt(0)
	s_barrier
	s_setprio 1
	s_waitcnt lgkmcnt(0)
	v_mfma_f32_16x16x32_bf16 v[128:131], v[148:151], v[180:183], v[128:131]
	v_mfma_f32_16x16x32_bf16 v[124:127], v[156:159], v[180:183], v[124:127]
	v_mfma_f32_16x16x32_bf16 v[120:123], v[148:151], v[188:191], v[120:123]
	v_mfma_f32_16x16x32_bf16 v[116:119], v[156:159], v[188:191], v[116:119]
	v_mfma_f32_16x16x32_bf16 v[108:111], v[148:151], v[196:199], v[108:111]
	v_mfma_f32_16x16x32_bf16 v[100:103], v[156:159], v[196:199], v[100:103]
	v_mfma_f32_16x16x32_bf16 v[92:95], v[148:151], v[204:207], v[92:95]
	v_mfma_f32_16x16x32_bf16 v[84:87], v[156:159], v[204:207], v[84:87]
	v_mfma_f32_16x16x32_bf16 v[128:131], v[152:155], v[184:187], v[128:131]
	v_mfma_f32_16x16x32_bf16 v[124:127], v[160:163], v[184:187], v[124:127]
	v_mfma_f32_16x16x32_bf16 v[120:123], v[152:155], v[192:195], v[120:123]
	v_mfma_f32_16x16x32_bf16 v[116:119], v[160:163], v[192:195], v[116:119]
	v_mfma_f32_16x16x32_bf16 v[108:111], v[152:155], v[200:203], v[108:111]
	v_mfma_f32_16x16x32_bf16 v[100:103], v[160:163], v[200:203], v[100:103]
	v_mfma_f32_16x16x32_bf16 v[92:95], v[152:155], v[208:211], v[92:95]
	v_mfma_f32_16x16x32_bf16 v[84:87], v[160:163], v[208:211], v[84:87]
	s_setprio 0
	s_setprio 1
	v_mfma_f32_16x16x32_bf16 v[112:115], v[164:167], v[180:183], v[112:115]
	v_mfma_f32_16x16x32_bf16 v[104:107], v[172:175], v[180:183], v[104:107]
	v_mfma_f32_16x16x32_bf16 v[96:99], v[164:167], v[188:191], v[96:99]
	v_mfma_f32_16x16x32_bf16 v[88:91], v[172:175], v[188:191], v[88:91]
	v_mfma_f32_16x16x32_bf16 v[80:83], v[164:167], v[196:199], v[80:83]
	v_mfma_f32_16x16x32_bf16 v[76:79], v[172:175], v[196:199], v[76:79]
	v_mfma_f32_16x16x32_bf16 v[72:75], v[164:167], v[204:207], v[72:75]
	v_mfma_f32_16x16x32_bf16 v[68:71], v[172:175], v[204:207], v[68:71]
	v_mfma_f32_16x16x32_bf16 v[112:115], v[168:171], v[184:187], v[112:115]
	v_mfma_f32_16x16x32_bf16 v[104:107], v[176:179], v[184:187], v[104:107]
	v_mfma_f32_16x16x32_bf16 v[96:99], v[168:171], v[192:195], v[96:99]
	v_mfma_f32_16x16x32_bf16 v[88:91], v[176:179], v[192:195], v[88:91]
	v_mfma_f32_16x16x32_bf16 v[80:83], v[168:171], v[200:203], v[80:83]
	v_mfma_f32_16x16x32_bf16 v[76:79], v[176:179], v[200:203], v[76:79]
	v_mfma_f32_16x16x32_bf16 v[72:75], v[168:171], v[208:211], v[72:75]
	v_mfma_f32_16x16x32_bf16 v[68:71], v[176:179], v[208:211], v[68:71]
	s_setprio 0
	s_barrier
	s_add_i32 s14, s16, s45
	v_lshl_add_u64 v[214:215], v[214:215], 0, s[28:29]
	s_mov_b32 m0, s14
	ds_read_b128 v[180:183], v146 offset:49152
	ds_read_b128 v[184:187], v146 offset:50176
	ds_read_b128 v[188:191], v146 offset:51200
	ds_read_b128 v[192:195], v146 offset:52224
	ds_read_b128 v[196:199], v146 offset:53248
	ds_read_b128 v[200:203], v146 offset:54272
	ds_read_b128 v[204:207], v146 offset:55296
	ds_read_b128 v[208:211], v146 offset:56320
	global_load_lds_dwordx4 v[214:215], off
	v_lshl_add_u64 v[214:215], v[216:217], 0, s[28:29]
	s_add_i32 m0, s14, 0x2000
	v_lshl_add_u64 v[212:213], v[212:213], 0, s[76:77]
	s_add_i32 s14, s69, s45
	global_load_lds_dwordx4 v[214:215], off
	v_lshl_add_u64 v[214:215], v[212:213], 0, v[132:133]
	s_mov_b32 m0, s14
	v_lshl_add_u64 v[212:213], v[212:213], 0, v[0:1]
	global_load_lds_dwordx4 v[214:215], off
	s_add_i32 m0, s14, 0x2000
	s_nop 0
	global_load_lds_dwordx4 v[212:213], off
	v_lshl_add_u64 v[212:213], v[218:219], 0, s[28:29]
	s_mov_b32 m0, s60
	s_nop 0
	global_load_lds_dwordx4 v[212:213], off
	v_lshl_add_u64 v[212:213], v[220:221], 0, s[28:29]
	s_mov_b32 m0, s61
	s_nop 0
	global_load_lds_dwordx4 v[212:213], off
	s_waitcnt vmcnt(8)
	s_waitcnt lgkmcnt(0)
	s_barrier
	s_setprio 1
	s_waitcnt lgkmcnt(0)
	v_mfma_f32_16x16x32_bf16 v[64:67], v[148:151], v[180:183], v[64:67]
	v_mfma_f32_16x16x32_bf16 v[60:63], v[156:159], v[180:183], v[60:63]
	v_mfma_f32_16x16x32_bf16 v[56:59], v[148:151], v[188:191], v[56:59]
	v_mfma_f32_16x16x32_bf16 v[52:55], v[156:159], v[188:191], v[52:55]
	v_mfma_f32_16x16x32_bf16 v[40:43], v[148:151], v[196:199], v[40:43]
	v_mfma_f32_16x16x32_bf16 v[36:39], v[156:159], v[196:199], v[36:39]
	v_mfma_f32_16x16x32_bf16 v[24:27], v[148:151], v[204:207], v[24:27]
	v_mfma_f32_16x16x32_bf16 v[20:23], v[156:159], v[204:207], v[20:23]
	v_mfma_f32_16x16x32_bf16 v[64:67], v[152:155], v[184:187], v[64:67]
	v_mfma_f32_16x16x32_bf16 v[60:63], v[160:163], v[184:187], v[60:63]
	v_mfma_f32_16x16x32_bf16 v[56:59], v[152:155], v[192:195], v[56:59]
	v_mfma_f32_16x16x32_bf16 v[52:55], v[160:163], v[192:195], v[52:55]
	v_mfma_f32_16x16x32_bf16 v[40:43], v[152:155], v[200:203], v[40:43]
	v_mfma_f32_16x16x32_bf16 v[36:39], v[160:163], v[200:203], v[36:39]
	v_mfma_f32_16x16x32_bf16 v[24:27], v[152:155], v[208:211], v[24:27]
	v_mfma_f32_16x16x32_bf16 v[20:23], v[160:163], v[208:211], v[20:23]
	s_setprio 0
	s_setprio 1
	v_mfma_f32_16x16x32_bf16 v[48:51], v[164:167], v[180:183], v[48:51]
	v_mfma_f32_16x16x32_bf16 v[44:47], v[172:175], v[180:183], v[44:47]
	v_mfma_f32_16x16x32_bf16 v[32:35], v[164:167], v[188:191], v[32:35]
	v_mfma_f32_16x16x32_bf16 v[28:31], v[172:175], v[188:191], v[28:31]
	v_mfma_f32_16x16x32_bf16 v[16:19], v[164:167], v[196:199], v[16:19]
	v_mfma_f32_16x16x32_bf16 v[12:15], v[172:175], v[196:199], v[12:15]
	v_mfma_f32_16x16x32_bf16 v[8:11], v[164:167], v[204:207], v[8:11]
	v_mfma_f32_16x16x32_bf16 v[4:7], v[172:175], v[204:207], v[4:7]
	v_mfma_f32_16x16x32_bf16 v[48:51], v[168:171], v[184:187], v[48:51]
	v_mfma_f32_16x16x32_bf16 v[44:47], v[176:179], v[184:187], v[44:47]
	v_mfma_f32_16x16x32_bf16 v[32:35], v[168:171], v[192:195], v[32:35]
	v_mfma_f32_16x16x32_bf16 v[28:31], v[176:179], v[192:195], v[28:31]
	v_mfma_f32_16x16x32_bf16 v[16:19], v[168:171], v[200:203], v[16:19]
	v_mfma_f32_16x16x32_bf16 v[12:15], v[176:179], v[200:203], v[12:15]
	v_mfma_f32_16x16x32_bf16 v[8:11], v[168:171], v[208:211], v[8:11]
	v_mfma_f32_16x16x32_bf16 v[4:7], v[176:179], v[208:211], v[4:7]
	s_setprio 0
	s_barrier
	v_lshl_add_u64 v[140:141], v[140:141], 0, s[70:71]
	s_cmp_ge_u32 s17, s57
	s_mov_b64 s[14:15], s[18:19]
	s_mov_b32 s16, s17
	s_cbranch_scc1 .Lmy_gx8
